# first-iteration peel of all nine GEMM K-loops: the peeled copy's first MFMA per accumulator tile takes SrcC=0, the 127 v_mov zeroing the accumulators before every K-loop are deleted (on top of p_mpost
# speedup vs baseline: 1.0109x; 1.0109x over previous
.LBB0_165:
	s_ashr_i32 s9, s8, 31
	s_lshl_b64 s[10:11], s[8:9], 20
	v_readlane_b32 s12, v254, 58
	v_readlane_b32 s13, v254, 59
	s_add_u32 s10, s12, s10
	s_addc_u32 s11, s13, s11
	s_and_b64 s[12:13], s[2:3], exec
	s_cselect_b32 s9, s11, s23
	s_cselect_b32 s49, s10, s22
	s_ashr_i32 s7, s6, 31
	s_lshl_b64 s[12:13], s[6:7], 20
	v_readlane_b32 s7, v255, 3
	s_add_u32 s12, s7, s12
	v_readlane_b32 s7, v255, 5
	s_addc_u32 s13, s7, s13
	s_and_b64 s[24:25], s[2:3], exec
	s_cselect_b32 s7, s13, s19
	s_cselect_b32 s50, s12, s18
	s_add_u32 s51, s18, 0x100
	s_addc_u32 s52, s19, 0
	s_add_u32 s18, s22, 0x80080
	v_mov_b32_e32 v6, 0
	s_addc_u32 s19, s23, 0
	s_mov_b32 s53, -2
	v_add_u32_e32 v142, s15, v144
	ds_read_b128 v[148:151], v142
	ds_read_b128 v[152:155], v142 offset:1024
	ds_read_b128 v[156:159], v142 offset:2048
	ds_read_b128 v[160:163], v142 offset:3072
	v_add_u32_e32 v142, s30, v144
	ds_read_b128 v[164:167], v142
	ds_read_b128 v[168:171], v142 offset:1024
	ds_read_b128 v[172:175], v142 offset:2048
	ds_read_b128 v[176:179], v142 offset:3072
	s_add_u32 s22, s18, 0xfff80080
	s_addc_u32 s23, s19, -1
	s_cmp_eq_u32 s53, 28
	s_cselect_b32 s25, s9, s23
	s_cselect_b32 s24, s49, s22
	s_cselect_b32 s23, s7, s52
	s_cselect_b32 s22, s50, s51
	v_lshl_add_u64 v[142:143], s[18:19], 0, v[140:141]
	s_add_i32 m0, s35, 0xc000
	ds_read_b128 v[180:183], v147
	ds_read_b128 v[184:187], v147 offset:1024
	ds_read_b128 v[188:191], v147 offset:2048
	ds_read_b128 v[192:195], v147 offset:3072
	ds_read_b128 v[196:199], v147 offset:4096
	ds_read_b128 v[206:209], v147 offset:5120
	ds_read_b128 v[210:213], v147 offset:6144
	ds_read_b128 v[214:217], v147 offset:7168
	global_load_lds_dwordx4 v[142:143], off
	v_lshl_add_u64 v[142:143], s[18:19], 0, v[138:139]
	s_add_i32 m0, s35, 0xe000
	s_nop 0
	global_load_lds_dwordx4 v[142:143], off
	s_waitcnt vmcnt(8)
	s_waitcnt lgkmcnt(0)
	s_barrier
	s_setprio 1
	s_waitcnt lgkmcnt(0)
	v_mfma_f32_16x16x32_bf16 v[130:133], v[148:151], v[180:183], 0
	v_mfma_f32_16x16x32_bf16 v[122:125], v[156:159], v[180:183], 0
	v_mfma_f32_16x16x32_bf16 v[114:117], v[148:151], v[188:191], 0
	v_mfma_f32_16x16x32_bf16 v[106:109], v[156:159], v[188:191], 0
	v_mfma_f32_16x16x32_bf16 v[98:101], v[148:151], v[196:199], 0
	v_mfma_f32_16x16x32_bf16 v[90:93], v[156:159], v[196:199], 0
	v_mfma_f32_16x16x32_bf16 v[82:85], v[148:151], v[210:213], 0
	v_mfma_f32_16x16x32_bf16 v[74:77], v[156:159], v[210:213], 0
	v_mfma_f32_16x16x32_bf16 v[130:133], v[152:155], v[184:187], v[130:133]
	v_mfma_f32_16x16x32_bf16 v[122:125], v[160:163], v[184:187], v[122:125]
	v_mfma_f32_16x16x32_bf16 v[114:117], v[152:155], v[192:195], v[114:117]
	v_mfma_f32_16x16x32_bf16 v[106:109], v[160:163], v[192:195], v[106:109]
	v_mfma_f32_16x16x32_bf16 v[98:101], v[152:155], v[206:209], v[98:101]
	v_mfma_f32_16x16x32_bf16 v[90:93], v[160:163], v[206:209], v[90:93]
	v_mfma_f32_16x16x32_bf16 v[82:85], v[152:155], v[214:217], v[82:85]
	v_mfma_f32_16x16x32_bf16 v[74:77], v[160:163], v[214:217], v[74:77]
	s_setprio 0
	s_setprio 1
	v_mfma_f32_16x16x32_bf16 v[126:129], v[164:167], v[180:183], 0
	v_mfma_f32_16x16x32_bf16 v[118:121], v[172:175], v[180:183], 0
	v_mfma_f32_16x16x32_bf16 v[110:113], v[164:167], v[188:191], 0
	v_mfma_f32_16x16x32_bf16 v[102:105], v[172:175], v[188:191], 0
	v_mfma_f32_16x16x32_bf16 v[94:97], v[164:167], v[196:199], 0
	v_mfma_f32_16x16x32_bf16 v[86:89], v[172:175], v[196:199], 0
	v_mfma_f32_16x16x32_bf16 v[78:81], v[164:167], v[210:213], 0
	v_mfma_f32_16x16x32_bf16 v[70:73], v[172:175], v[210:213], 0
	v_mfma_f32_16x16x32_bf16 v[126:129], v[168:171], v[184:187], v[126:129]
	v_mfma_f32_16x16x32_bf16 v[118:121], v[176:179], v[184:187], v[118:121]
	v_mfma_f32_16x16x32_bf16 v[110:113], v[168:171], v[192:195], v[110:113]
	v_mfma_f32_16x16x32_bf16 v[102:105], v[176:179], v[192:195], v[102:105]
	v_mfma_f32_16x16x32_bf16 v[94:97], v[168:171], v[206:209], v[94:97]
	v_mfma_f32_16x16x32_bf16 v[86:89], v[176:179], v[206:209], v[86:89]
	s_setprio 2
	s_barrier
	v_mfma_f32_16x16x32_bf16 v[78:81], v[168:171], v[214:217], v[78:81]
	v_mfma_f32_16x16x32_bf16 v[70:73], v[176:179], v[214:217], v[70:73]
	s_setprio 0
	s_mov_b32 m0, s20
	v_lshl_add_u64 v[142:143], s[22:23], 0, v[0:1]
	s_add_u32 s54, s22, 0x80000
	ds_read_b128 v[180:183], v147 offset:16384
	ds_read_b128 v[184:187], v147 offset:17408
	ds_read_b128 v[188:191], v147 offset:18432
	ds_read_b128 v[192:195], v147 offset:19456
	ds_read_b128 v[196:199], v147 offset:20480
	ds_read_b128 v[206:209], v147 offset:21504
	ds_read_b128 v[210:213], v147 offset:22528
	ds_read_b128 v[214:217], v147 offset:23552
	global_load_lds_dwordx4 v[142:143], off
	v_lshl_add_u64 v[200:201], s[22:23], 0, v[2:3]
	s_mov_b32 m0, s26
	s_addc_u32 s55, s23, 0
	global_load_lds_dwordx4 v[200:201], off
	v_lshl_add_u64 v[218:219], s[54:55], 0, v[0:1]
	s_mov_b32 m0, s31
	v_lshl_add_u64 v[220:221], s[24:25], 0, v[134:135]
	global_load_lds_dwordx4 v[218:219], off
	v_lshl_add_u64 v[218:219], s[54:55], 0, v[2:3]
	s_mov_b32 m0, s34
	s_nop 0
	global_load_lds_dwordx4 v[218:219], off
	v_lshl_add_u64 v[218:219], s[24:25], 0, v[136:137]
	s_mov_b32 m0, s35
	s_nop 0
	global_load_lds_dwordx4 v[218:219], off
	s_mov_b32 m0, s36
	s_nop 0
	global_load_lds_dwordx4 v[220:221], off
	s_waitcnt vmcnt(8)
	s_waitcnt lgkmcnt(0)
	s_barrier
	s_setprio 1
	s_waitcnt lgkmcnt(0)
	v_mfma_f32_16x16x32_bf16 v[66:69], v[148:151], v[180:183], 0
	v_mfma_f32_16x16x32_bf16 v[58:61], v[156:159], v[180:183], 0
	v_mfma_f32_16x16x32_bf16 v[50:53], v[148:151], v[188:191], 0
	v_mfma_f32_16x16x32_bf16 v[42:45], v[156:159], v[188:191], 0
	v_mfma_f32_16x16x32_bf16 v[34:37], v[148:151], v[196:199], 0
	v_mfma_f32_16x16x32_bf16 v[26:29], v[156:159], v[196:199], 0
	v_mfma_f32_16x16x32_bf16 v[18:21], v[148:151], v[210:213], 0
	v_mfma_f32_16x16x32_bf16 v[10:13], v[156:159], v[210:213], 0
	v_mfma_f32_16x16x32_bf16 v[66:69], v[152:155], v[184:187], v[66:69]
	v_mfma_f32_16x16x32_bf16 v[58:61], v[160:163], v[184:187], v[58:61]
	v_mfma_f32_16x16x32_bf16 v[50:53], v[152:155], v[192:195], v[50:53]
	v_mfma_f32_16x16x32_bf16 v[42:45], v[160:163], v[192:195], v[42:45]
	v_mfma_f32_16x16x32_bf16 v[34:37], v[152:155], v[206:209], v[34:37]
	v_mfma_f32_16x16x32_bf16 v[26:29], v[160:163], v[206:209], v[26:29]
	v_mfma_f32_16x16x32_bf16 v[18:21], v[152:155], v[214:217], v[18:21]
	v_mfma_f32_16x16x32_bf16 v[10:13], v[160:163], v[214:217], v[10:13]
	s_setprio 0
	s_setprio 1
	v_mfma_f32_16x16x32_bf16 v[62:65], v[164:167], v[180:183], 0
	v_mfma_f32_16x16x32_bf16 v[54:57], v[172:175], v[180:183], 0
	v_mfma_f32_16x16x32_bf16 v[46:49], v[164:167], v[188:191], 0
	v_mfma_f32_16x16x32_bf16 v[38:41], v[172:175], v[188:191], 0
	v_mfma_f32_16x16x32_bf16 v[30:33], v[164:167], v[196:199], 0
	v_mfma_f32_16x16x32_bf16 v[22:25], v[172:175], v[196:199], 0
	v_mfma_f32_16x16x32_bf16 v[14:17], v[164:167], v[210:213], 0
	v_mfma_f32_16x16x32_bf16 v[6:9], v[172:175], v[210:213], 0
	v_mfma_f32_16x16x32_bf16 v[62:65], v[168:171], v[184:187], v[62:65]
	v_mfma_f32_16x16x32_bf16 v[54:57], v[176:179], v[184:187], v[54:57]
	v_mfma_f32_16x16x32_bf16 v[46:49], v[168:171], v[192:195], v[46:49]
	v_mfma_f32_16x16x32_bf16 v[38:41], v[176:179], v[192:195], v[38:41]
	v_mfma_f32_16x16x32_bf16 v[30:33], v[168:171], v[206:209], v[30:33]
	v_mfma_f32_16x16x32_bf16 v[22:25], v[176:179], v[206:209], v[22:25]
	s_setprio 2
	s_barrier
	v_mfma_f32_16x16x32_bf16 v[14:17], v[168:171], v[214:217], v[14:17]
	v_mfma_f32_16x16x32_bf16 v[6:9], v[176:179], v[214:217], v[6:9]
	s_setprio 0
	v_add_u32_e32 v160, s39, v144
	v_add_u32_e32 v176, s44, v144
	ds_read_b128 v[148:151], v160
	ds_read_b128 v[152:155], v160 offset:1024
	ds_read_b128 v[156:159], v160 offset:2048
	ds_read_b128 v[160:163], v160 offset:3072
	ds_read_b128 v[164:167], v176
	ds_read_b128 v[168:171], v176 offset:1024
	ds_read_b128 v[172:175], v176 offset:2048
	ds_read_b128 v[176:179], v176 offset:3072
	s_add_u32 s24, s24, 0x80000
	s_addc_u32 s25, s25, 0
	s_mov_b32 m0, s37
	v_lshl_add_u64 v[222:223], s[24:25], 0, v[136:137]
	ds_read_b128 v[180:183], v147 offset:32768
	ds_read_b128 v[184:187], v147 offset:33792
	ds_read_b128 v[188:191], v147 offset:34816
	ds_read_b128 v[192:195], v147 offset:35840
	ds_read_b128 v[196:199], v147 offset:36864
	ds_read_b128 v[206:209], v147 offset:37888
	ds_read_b128 v[210:213], v147 offset:38912
	ds_read_b128 v[214:217], v147 offset:39936
	global_load_lds_dwordx4 v[222:223], off
	v_lshl_add_u64 v[222:223], s[24:25], 0, v[134:135]
	s_mov_b32 m0, s38
	s_nop 0
	global_load_lds_dwordx4 v[222:223], off
	s_waitcnt vmcnt(8)
	s_waitcnt lgkmcnt(0)
	s_barrier
	s_setprio 1
	s_waitcnt lgkmcnt(0)
	v_mfma_f32_16x16x32_bf16 v[130:133], v[148:151], v[180:183], v[130:133]
	v_mfma_f32_16x16x32_bf16 v[122:125], v[156:159], v[180:183], v[122:125]
	v_mfma_f32_16x16x32_bf16 v[114:117], v[148:151], v[188:191], v[114:117]
	v_mfma_f32_16x16x32_bf16 v[106:109], v[156:159], v[188:191], v[106:109]
	v_mfma_f32_16x16x32_bf16 v[98:101], v[148:151], v[196:199], v[98:101]
	v_mfma_f32_16x16x32_bf16 v[90:93], v[156:159], v[196:199], v[90:93]
	v_mfma_f32_16x16x32_bf16 v[82:85], v[148:151], v[210:213], v[82:85]
	v_mfma_f32_16x16x32_bf16 v[74:77], v[156:159], v[210:213], v[74:77]
	v_mfma_f32_16x16x32_bf16 v[130:133], v[152:155], v[184:187], v[130:133]
	v_mfma_f32_16x16x32_bf16 v[122:125], v[160:163], v[184:187], v[122:125]
	v_mfma_f32_16x16x32_bf16 v[114:117], v[152:155], v[192:195], v[114:117]
	v_mfma_f32_16x16x32_bf16 v[106:109], v[160:163], v[192:195], v[106:109]
	v_mfma_f32_16x16x32_bf16 v[98:101], v[152:155], v[206:209], v[98:101]
	v_mfma_f32_16x16x32_bf16 v[90:93], v[160:163], v[206:209], v[90:93]
	v_mfma_f32_16x16x32_bf16 v[82:85], v[152:155], v[214:217], v[82:85]
	v_mfma_f32_16x16x32_bf16 v[74:77], v[160:163], v[214:217], v[74:77]
	s_setprio 0
	s_setprio 1
	v_mfma_f32_16x16x32_bf16 v[126:129], v[164:167], v[180:183], v[126:129]
	v_mfma_f32_16x16x32_bf16 v[118:121], v[172:175], v[180:183], v[118:121]
	v_mfma_f32_16x16x32_bf16 v[110:113], v[164:167], v[188:191], v[110:113]
	v_mfma_f32_16x16x32_bf16 v[102:105], v[172:175], v[188:191], v[102:105]
	v_mfma_f32_16x16x32_bf16 v[94:97], v[164:167], v[196:199], v[94:97]
	v_mfma_f32_16x16x32_bf16 v[86:89], v[172:175], v[196:199], v[86:89]
	v_mfma_f32_16x16x32_bf16 v[78:81], v[164:167], v[210:213], v[78:81]
	v_mfma_f32_16x16x32_bf16 v[70:73], v[172:175], v[210:213], v[70:73]
	v_mfma_f32_16x16x32_bf16 v[126:129], v[168:171], v[184:187], v[126:129]
	v_mfma_f32_16x16x32_bf16 v[118:121], v[176:179], v[184:187], v[118:121]
	v_mfma_f32_16x16x32_bf16 v[110:113], v[168:171], v[192:195], v[110:113]
	v_mfma_f32_16x16x32_bf16 v[102:105], v[176:179], v[192:195], v[102:105]
	v_mfma_f32_16x16x32_bf16 v[94:97], v[168:171], v[206:209], v[94:97]
	v_mfma_f32_16x16x32_bf16 v[86:89], v[176:179], v[206:209], v[86:89]
	s_setprio 2
	s_barrier
	v_mfma_f32_16x16x32_bf16 v[78:81], v[168:171], v[214:217], v[78:81]
	v_mfma_f32_16x16x32_bf16 v[70:73], v[176:179], v[214:217], v[70:73]
	s_setprio 0
	s_mov_b32 m0, s40
	v_lshl_add_u64 v[142:143], v[142:143], 0, s[28:29]
	s_add_u32 s22, s22, 0x80080
	ds_read_b128 v[180:183], v147 offset:49152
	ds_read_b128 v[184:187], v147 offset:50176
	ds_read_b128 v[188:191], v147 offset:51200
	ds_read_b128 v[192:195], v147 offset:52224
	ds_read_b128 v[196:199], v147 offset:53248
	ds_read_b128 v[206:209], v147 offset:54272
	ds_read_b128 v[210:213], v147 offset:55296
	ds_read_b128 v[214:217], v147 offset:56320
	global_load_lds_dwordx4 v[142:143], off
	v_lshl_add_u64 v[142:143], v[200:201], 0, s[28:29]
	s_mov_b32 m0, s41
	s_addc_u32 s23, s23, 0
	global_load_lds_dwordx4 v[142:143], off
	v_lshl_add_u64 v[142:143], s[22:23], 0, v[0:1]
	s_mov_b32 m0, s45
	s_nop 0
	global_load_lds_dwordx4 v[142:143], off
	v_lshl_add_u64 v[142:143], s[22:23], 0, v[2:3]
	s_mov_b32 m0, s46
	s_nop 0
	global_load_lds_dwordx4 v[142:143], off
	v_lshl_add_u64 v[142:143], v[218:219], 0, s[28:29]
	s_mov_b32 m0, s42
	s_nop 0
	global_load_lds_dwordx4 v[142:143], off
	v_lshl_add_u64 v[142:143], v[220:221], 0, s[28:29]
	s_mov_b32 m0, s43
	s_nop 0
	global_load_lds_dwordx4 v[142:143], off
	s_waitcnt vmcnt(8)
	s_waitcnt lgkmcnt(0)
	s_barrier
	s_setprio 1
	s_waitcnt lgkmcnt(0)
	v_mfma_f32_16x16x32_bf16 v[66:69], v[148:151], v[180:183], v[66:69]
	v_mfma_f32_16x16x32_bf16 v[58:61], v[156:159], v[180:183], v[58:61]
	v_mfma_f32_16x16x32_bf16 v[50:53], v[148:151], v[188:191], v[50:53]
	v_mfma_f32_16x16x32_bf16 v[42:45], v[156:159], v[188:191], v[42:45]
	v_mfma_f32_16x16x32_bf16 v[34:37], v[148:151], v[196:199], v[34:37]
	v_mfma_f32_16x16x32_bf16 v[26:29], v[156:159], v[196:199], v[26:29]
	v_mfma_f32_16x16x32_bf16 v[18:21], v[148:151], v[210:213], v[18:21]
	v_mfma_f32_16x16x32_bf16 v[10:13], v[156:159], v[210:213], v[10:13]
	v_mfma_f32_16x16x32_bf16 v[66:69], v[152:155], v[184:187], v[66:69]
	v_mfma_f32_16x16x32_bf16 v[58:61], v[160:163], v[184:187], v[58:61]
	v_mfma_f32_16x16x32_bf16 v[50:53], v[152:155], v[192:195], v[50:53]
	v_mfma_f32_16x16x32_bf16 v[42:45], v[160:163], v[192:195], v[42:45]
	v_mfma_f32_16x16x32_bf16 v[34:37], v[152:155], v[206:209], v[34:37]
	v_mfma_f32_16x16x32_bf16 v[26:29], v[160:163], v[206:209], v[26:29]
	v_mfma_f32_16x16x32_bf16 v[18:21], v[152:155], v[214:217], v[18:21]
	v_mfma_f32_16x16x32_bf16 v[10:13], v[160:163], v[214:217], v[10:13]
	s_setprio 0
	s_setprio 1
	v_mfma_f32_16x16x32_bf16 v[62:65], v[164:167], v[180:183], v[62:65]
	v_mfma_f32_16x16x32_bf16 v[54:57], v[172:175], v[180:183], v[54:57]
	v_mfma_f32_16x16x32_bf16 v[46:49], v[164:167], v[188:191], v[46:49]
	v_mfma_f32_16x16x32_bf16 v[38:41], v[172:175], v[188:191], v[38:41]
	v_mfma_f32_16x16x32_bf16 v[30:33], v[164:167], v[196:199], v[30:33]
	v_mfma_f32_16x16x32_bf16 v[22:25], v[172:175], v[196:199], v[22:25]
	v_mfma_f32_16x16x32_bf16 v[14:17], v[164:167], v[210:213], v[14:17]
	v_mfma_f32_16x16x32_bf16 v[6:9], v[172:175], v[210:213], v[6:9]
	v_mfma_f32_16x16x32_bf16 v[62:65], v[168:171], v[184:187], v[62:65]
	v_mfma_f32_16x16x32_bf16 v[54:57], v[176:179], v[184:187], v[54:57]
	v_mfma_f32_16x16x32_bf16 v[46:49], v[168:171], v[192:195], v[46:49]
	v_mfma_f32_16x16x32_bf16 v[38:41], v[176:179], v[192:195], v[38:41]
	v_mfma_f32_16x16x32_bf16 v[30:33], v[168:171], v[206:209], v[30:33]
	v_mfma_f32_16x16x32_bf16 v[22:25], v[176:179], v[206:209], v[22:25]
	s_setprio 2
	s_barrier
	v_mfma_f32_16x16x32_bf16 v[14:17], v[168:171], v[214:217], v[14:17]
	v_mfma_f32_16x16x32_bf16 v[6:9], v[176:179], v[214:217], v[6:9]
	s_setprio 0
	s_add_i32 s53, s53, 2
	s_add_u32 s51, s51, 0x100
	s_addc_u32 s52, s52, 0
	s_add_u32 s18, s18, 0x100
	s_addc_u32 s19, s19, 0
	s_cmp_gt_u32 s53, 29
	s_cbranch_scc0 .LBB0_166
	s_branch .Lpeel_x__166

.Lpeel_x__166:
	s_and_b64 vcc, exec, s[4:5]
	s_cbranch_vccz .LBB0_169
	s_barrier

.LBB0_245:
	s_add_u32 s54, s10, 0x100
	v_mov_b32_e32 v6, 0
	s_addc_u32 s55, s11, 0
	s_mov_b32 s56, -2
	s_waitcnt lgkmcnt(0)
	v_add_u32_e32 v146, s19, v182
	v_add_u32_e32 v170, s23, v182
	ds_read_b128 v[134:137], v146
	ds_read_b128 v[138:141], v146 offset:1024
	ds_read_b128 v[142:145], v146 offset:2048
	ds_read_b128 v[146:149], v146 offset:3072
	ds_read_b128 v[150:153], v170
	ds_read_b128 v[154:157], v170 offset:1024
	ds_read_b128 v[158:161], v170 offset:2048
	ds_read_b128 v[170:173], v170 offset:3072
	s_add_u32 s10, s8, 0x100
	s_addc_u32 s11, s9, 0
	s_cmpk_eq_i32 s56, 0x52
	s_cselect_b32 s15, s3, s11
	s_cselect_b32 s14, s2, s10
	s_cselect_b32 s13, s7, s55
	s_cselect_b32 s12, s6, s54
	v_lshl_add_u64 v[214:215], s[8:9], 0, v[168:169]
	s_add_i32 m0, s30, 0xc000
	ds_read_b128 v[174:177], v184
	ds_read_b128 v[178:181], v184 offset:1024
	ds_read_b128 v[186:189], v184 offset:2048
	ds_read_b128 v[190:193], v184 offset:3072
	ds_read_b128 v[194:197], v184 offset:4096
	ds_read_b128 v[198:201], v184 offset:5120
	ds_read_b128 v[206:209], v184 offset:6144
	ds_read_b128 v[210:213], v184 offset:7168
	global_load_lds_dwordx4 v[214:215], off
	v_lshl_add_u64 v[214:215], s[8:9], 0, v[166:167]
	s_add_i32 m0, s30, 0xe000
	s_nop 0
	global_load_lds_dwordx4 v[214:215], off
	s_waitcnt vmcnt(8)
	s_waitcnt lgkmcnt(0)
	s_barrier
	s_setprio 1
	s_waitcnt lgkmcnt(0)
	v_mfma_f32_16x16x32_bf16 v[130:133], v[134:137], v[174:177], 0
	v_mfma_f32_16x16x32_bf16 v[126:129], v[142:145], v[174:177], 0
	v_mfma_f32_16x16x32_bf16 v[114:117], v[134:137], v[186:189], 0
	v_mfma_f32_16x16x32_bf16 v[110:113], v[142:145], v[186:189], 0
	v_mfma_f32_16x16x32_bf16 v[98:101], v[134:137], v[194:197], 0
	v_mfma_f32_16x16x32_bf16 v[94:97], v[142:145], v[194:197], 0
	v_mfma_f32_16x16x32_bf16 v[82:85], v[134:137], v[206:209], 0
	v_mfma_f32_16x16x32_bf16 v[78:81], v[142:145], v[206:209], 0
	v_mfma_f32_16x16x32_bf16 v[130:133], v[138:141], v[178:181], v[130:133]
	v_mfma_f32_16x16x32_bf16 v[126:129], v[146:149], v[178:181], v[126:129]
	v_mfma_f32_16x16x32_bf16 v[114:117], v[138:141], v[190:193], v[114:117]
	v_mfma_f32_16x16x32_bf16 v[110:113], v[146:149], v[190:193], v[110:113]
	v_mfma_f32_16x16x32_bf16 v[98:101], v[138:141], v[198:201], v[98:101]
	v_mfma_f32_16x16x32_bf16 v[94:97], v[146:149], v[198:201], v[94:97]
	v_mfma_f32_16x16x32_bf16 v[82:85], v[138:141], v[210:213], v[82:85]
	v_mfma_f32_16x16x32_bf16 v[78:81], v[146:149], v[210:213], v[78:81]
	s_setprio 0
	s_setprio 1
	v_mfma_f32_16x16x32_bf16 v[122:125], v[150:153], v[174:177], 0
	v_mfma_f32_16x16x32_bf16 v[118:121], v[158:161], v[174:177], 0
	v_mfma_f32_16x16x32_bf16 v[106:109], v[150:153], v[186:189], 0
	v_mfma_f32_16x16x32_bf16 v[102:105], v[158:161], v[186:189], 0
	v_mfma_f32_16x16x32_bf16 v[90:93], v[150:153], v[194:197], 0
	v_mfma_f32_16x16x32_bf16 v[86:89], v[158:161], v[194:197], 0
	v_mfma_f32_16x16x32_bf16 v[74:77], v[150:153], v[206:209], 0
	v_mfma_f32_16x16x32_bf16 v[70:73], v[158:161], v[206:209], 0
	v_mfma_f32_16x16x32_bf16 v[122:125], v[154:157], v[178:181], v[122:125]
	v_mfma_f32_16x16x32_bf16 v[118:121], v[170:173], v[178:181], v[118:121]
	v_mfma_f32_16x16x32_bf16 v[106:109], v[154:157], v[190:193], v[106:109]
	v_mfma_f32_16x16x32_bf16 v[102:105], v[170:173], v[190:193], v[102:105]
	v_mfma_f32_16x16x32_bf16 v[90:93], v[154:157], v[198:201], v[90:93]
	v_mfma_f32_16x16x32_bf16 v[86:89], v[170:173], v[198:201], v[86:89]
	s_setprio 2
	s_barrier
	v_mfma_f32_16x16x32_bf16 v[74:77], v[154:157], v[210:213], v[74:77]
	v_mfma_f32_16x16x32_bf16 v[70:73], v[170:173], v[210:213], v[70:73]
	s_setprio 0
	s_mov_b32 m0, s20
	v_lshl_add_u64 v[214:215], s[12:13], 0, v[0:1]
	s_add_u32 s8, s12, 0x158000
	ds_read_b128 v[174:177], v184 offset:16384
	ds_read_b128 v[178:181], v184 offset:17408
	ds_read_b128 v[186:189], v184 offset:18432
	ds_read_b128 v[190:193], v184 offset:19456
	ds_read_b128 v[194:197], v184 offset:20480
	ds_read_b128 v[198:201], v184 offset:21504
	ds_read_b128 v[206:209], v184 offset:22528
	ds_read_b128 v[210:213], v184 offset:23552
	global_load_lds_dwordx4 v[214:215], off
	v_lshl_add_u64 v[216:217], s[12:13], 0, v[164:165]
	s_mov_b32 m0, s22
	s_addc_u32 s9, s13, 0
	global_load_lds_dwordx4 v[216:217], off
	v_lshl_add_u64 v[218:219], s[8:9], 0, v[0:1]
	s_mov_b32 m0, s24
	v_lshl_add_u64 v[220:221], s[14:15], 0, v[162:163]
	global_load_lds_dwordx4 v[218:219], off
	v_lshl_add_u64 v[218:219], s[8:9], 0, v[164:165]
	s_mov_b32 m0, s25
	s_nop 0
	global_load_lds_dwordx4 v[218:219], off
	v_lshl_add_u64 v[218:219], s[14:15], 0, v[2:3]
	s_mov_b32 m0, s30
	s_nop 0
	global_load_lds_dwordx4 v[218:219], off
	s_mov_b32 m0, s31
	s_nop 0
	global_load_lds_dwordx4 v[220:221], off
	s_waitcnt vmcnt(8)
	s_waitcnt lgkmcnt(0)
	s_barrier
	s_setprio 1
	s_waitcnt lgkmcnt(0)
	v_mfma_f32_16x16x32_bf16 v[66:69], v[134:137], v[174:177], 0
	v_mfma_f32_16x16x32_bf16 v[62:65], v[142:145], v[174:177], 0
	v_mfma_f32_16x16x32_bf16 v[50:53], v[134:137], v[186:189], 0
	v_mfma_f32_16x16x32_bf16 v[46:49], v[142:145], v[186:189], 0
	v_mfma_f32_16x16x32_bf16 v[34:37], v[134:137], v[194:197], 0
	v_mfma_f32_16x16x32_bf16 v[30:33], v[142:145], v[194:197], 0
	v_mfma_f32_16x16x32_bf16 v[18:21], v[134:137], v[206:209], 0
	v_mfma_f32_16x16x32_bf16 v[14:17], v[142:145], v[206:209], 0
	v_mfma_f32_16x16x32_bf16 v[66:69], v[138:141], v[178:181], v[66:69]
	v_mfma_f32_16x16x32_bf16 v[62:65], v[146:149], v[178:181], v[62:65]
	v_mfma_f32_16x16x32_bf16 v[50:53], v[138:141], v[190:193], v[50:53]
	v_mfma_f32_16x16x32_bf16 v[46:49], v[146:149], v[190:193], v[46:49]
	v_mfma_f32_16x16x32_bf16 v[34:37], v[138:141], v[198:201], v[34:37]
	v_mfma_f32_16x16x32_bf16 v[30:33], v[146:149], v[198:201], v[30:33]
	v_mfma_f32_16x16x32_bf16 v[18:21], v[138:141], v[210:213], v[18:21]
	v_mfma_f32_16x16x32_bf16 v[14:17], v[146:149], v[210:213], v[14:17]
	s_setprio 0
	s_setprio 1
	v_mfma_f32_16x16x32_bf16 v[58:61], v[150:153], v[174:177], 0
	v_mfma_f32_16x16x32_bf16 v[54:57], v[158:161], v[174:177], 0
	v_mfma_f32_16x16x32_bf16 v[42:45], v[150:153], v[186:189], 0
	v_mfma_f32_16x16x32_bf16 v[38:41], v[158:161], v[186:189], 0
	v_mfma_f32_16x16x32_bf16 v[26:29], v[150:153], v[194:197], 0
	v_mfma_f32_16x16x32_bf16 v[22:25], v[158:161], v[194:197], 0
	v_mfma_f32_16x16x32_bf16 v[10:13], v[150:153], v[206:209], 0
	v_mfma_f32_16x16x32_bf16 v[6:9], v[158:161], v[206:209], 0
	v_mfma_f32_16x16x32_bf16 v[58:61], v[154:157], v[178:181], v[58:61]
	v_mfma_f32_16x16x32_bf16 v[54:57], v[170:173], v[178:181], v[54:57]
	v_mfma_f32_16x16x32_bf16 v[42:45], v[154:157], v[190:193], v[42:45]
	v_mfma_f32_16x16x32_bf16 v[38:41], v[170:173], v[190:193], v[38:41]
	v_mfma_f32_16x16x32_bf16 v[26:29], v[154:157], v[198:201], v[26:29]
	v_mfma_f32_16x16x32_bf16 v[22:25], v[170:173], v[198:201], v[22:25]
	s_setprio 2
	s_barrier
	v_mfma_f32_16x16x32_bf16 v[10:13], v[154:157], v[210:213], v[10:13]
	v_mfma_f32_16x16x32_bf16 v[6:9], v[170:173], v[210:213], v[6:9]
	s_setprio 0
	v_add_u32_e32 v146, s41, v182
	v_add_u32_e32 v170, s46, v182
	ds_read_b128 v[134:137], v146
	ds_read_b128 v[138:141], v146 offset:1024
	ds_read_b128 v[142:145], v146 offset:2048
	ds_read_b128 v[146:149], v146 offset:3072
	ds_read_b128 v[150:153], v170
	ds_read_b128 v[154:157], v170 offset:1024
	ds_read_b128 v[158:161], v170 offset:2048
	ds_read_b128 v[170:173], v170 offset:3072
	s_add_u32 s8, s14, 0x280000
	s_addc_u32 s9, s15, 0
	s_mov_b32 m0, s34
	v_lshl_add_u64 v[222:223], s[8:9], 0, v[2:3]
	ds_read_b128 v[174:177], v184 offset:32768
	ds_read_b128 v[178:181], v184 offset:33792
	ds_read_b128 v[186:189], v184 offset:34816
	ds_read_b128 v[190:193], v184 offset:35840
	ds_read_b128 v[194:197], v184 offset:36864
	ds_read_b128 v[198:201], v184 offset:37888
	ds_read_b128 v[206:209], v184 offset:38912
	ds_read_b128 v[210:213], v184 offset:39936
	global_load_lds_dwordx4 v[222:223], off
	v_lshl_add_u64 v[222:223], s[8:9], 0, v[162:163]
	s_mov_b32 m0, s35
	s_nop 0
	global_load_lds_dwordx4 v[222:223], off
	s_waitcnt vmcnt(8)
	s_waitcnt lgkmcnt(0)
	s_barrier
	s_setprio 1
	s_waitcnt lgkmcnt(0)
	v_mfma_f32_16x16x32_bf16 v[130:133], v[134:137], v[174:177], v[130:133]
	v_mfma_f32_16x16x32_bf16 v[126:129], v[142:145], v[174:177], v[126:129]
	v_mfma_f32_16x16x32_bf16 v[114:117], v[134:137], v[186:189], v[114:117]
	v_mfma_f32_16x16x32_bf16 v[110:113], v[142:145], v[186:189], v[110:113]
	v_mfma_f32_16x16x32_bf16 v[98:101], v[134:137], v[194:197], v[98:101]
	v_mfma_f32_16x16x32_bf16 v[94:97], v[142:145], v[194:197], v[94:97]
	v_mfma_f32_16x16x32_bf16 v[82:85], v[134:137], v[206:209], v[82:85]
	v_mfma_f32_16x16x32_bf16 v[78:81], v[142:145], v[206:209], v[78:81]
	v_mfma_f32_16x16x32_bf16 v[130:133], v[138:141], v[178:181], v[130:133]
	v_mfma_f32_16x16x32_bf16 v[126:129], v[146:149], v[178:181], v[126:129]
	v_mfma_f32_16x16x32_bf16 v[114:117], v[138:141], v[190:193], v[114:117]
	v_mfma_f32_16x16x32_bf16 v[110:113], v[146:149], v[190:193], v[110:113]
	v_mfma_f32_16x16x32_bf16 v[98:101], v[138:141], v[198:201], v[98:101]
	v_mfma_f32_16x16x32_bf16 v[94:97], v[146:149], v[198:201], v[94:97]
	v_mfma_f32_16x16x32_bf16 v[82:85], v[138:141], v[210:213], v[82:85]
	v_mfma_f32_16x16x32_bf16 v[78:81], v[146:149], v[210:213], v[78:81]
	s_setprio 0
	s_setprio 1
	v_mfma_f32_16x16x32_bf16 v[122:125], v[150:153], v[174:177], v[122:125]
	v_mfma_f32_16x16x32_bf16 v[118:121], v[158:161], v[174:177], v[118:121]
	v_mfma_f32_16x16x32_bf16 v[106:109], v[150:153], v[186:189], v[106:109]
	v_mfma_f32_16x16x32_bf16 v[102:105], v[158:161], v[186:189], v[102:105]
	v_mfma_f32_16x16x32_bf16 v[90:93], v[150:153], v[194:197], v[90:93]
	v_mfma_f32_16x16x32_bf16 v[86:89], v[158:161], v[194:197], v[86:89]
	v_mfma_f32_16x16x32_bf16 v[74:77], v[150:153], v[206:209], v[74:77]
	v_mfma_f32_16x16x32_bf16 v[70:73], v[158:161], v[206:209], v[70:73]
	v_mfma_f32_16x16x32_bf16 v[122:125], v[154:157], v[178:181], v[122:125]
	v_mfma_f32_16x16x32_bf16 v[118:121], v[170:173], v[178:181], v[118:121]
	v_mfma_f32_16x16x32_bf16 v[106:109], v[154:157], v[190:193], v[106:109]
	v_mfma_f32_16x16x32_bf16 v[102:105], v[170:173], v[190:193], v[102:105]
	v_mfma_f32_16x16x32_bf16 v[90:93], v[154:157], v[198:201], v[90:93]
	v_mfma_f32_16x16x32_bf16 v[86:89], v[170:173], v[198:201], v[86:89]
	s_setprio 2
	s_barrier
	v_mfma_f32_16x16x32_bf16 v[74:77], v[154:157], v[210:213], v[74:77]
	v_mfma_f32_16x16x32_bf16 v[70:73], v[170:173], v[210:213], v[70:73]
	s_setprio 0
	s_mov_b32 m0, s42
	v_lshl_add_u64 v[214:215], v[214:215], 0, s[28:29]
	s_add_u32 s8, s12, 0x158080
	ds_read_b128 v[174:177], v184 offset:49152
	ds_read_b128 v[178:181], v184 offset:50176
	ds_read_b128 v[186:189], v184 offset:51200
	ds_read_b128 v[190:193], v184 offset:52224
	ds_read_b128 v[194:197], v184 offset:53248
	ds_read_b128 v[198:201], v184 offset:54272
	ds_read_b128 v[206:209], v184 offset:55296
	ds_read_b128 v[210:213], v184 offset:56320
	global_load_lds_dwordx4 v[214:215], off
	v_lshl_add_u64 v[214:215], v[216:217], 0, s[28:29]
	s_mov_b32 m0, s43
	s_addc_u32 s9, s13, 0
	global_load_lds_dwordx4 v[214:215], off
	v_lshl_add_u64 v[214:215], s[8:9], 0, v[0:1]
	s_mov_b32 m0, s47
	s_nop 0
	global_load_lds_dwordx4 v[214:215], off
	v_lshl_add_u64 v[214:215], s[8:9], 0, v[164:165]
	s_mov_b32 m0, s48
	s_nop 0
	global_load_lds_dwordx4 v[214:215], off
	v_lshl_add_u64 v[214:215], v[218:219], 0, s[28:29]
	s_mov_b32 m0, s44
	s_nop 0
	global_load_lds_dwordx4 v[214:215], off
	v_lshl_add_u64 v[214:215], v[220:221], 0, s[28:29]
	s_mov_b32 m0, s45
	s_nop 0
	global_load_lds_dwordx4 v[214:215], off
	s_waitcnt vmcnt(8)
	s_waitcnt lgkmcnt(0)
	s_barrier
	s_setprio 1
	s_waitcnt lgkmcnt(0)
	v_mfma_f32_16x16x32_bf16 v[66:69], v[134:137], v[174:177], v[66:69]
	v_mfma_f32_16x16x32_bf16 v[62:65], v[142:145], v[174:177], v[62:65]
	v_mfma_f32_16x16x32_bf16 v[50:53], v[134:137], v[186:189], v[50:53]
	v_mfma_f32_16x16x32_bf16 v[46:49], v[142:145], v[186:189], v[46:49]
	v_mfma_f32_16x16x32_bf16 v[34:37], v[134:137], v[194:197], v[34:37]
	v_mfma_f32_16x16x32_bf16 v[30:33], v[142:145], v[194:197], v[30:33]
	v_mfma_f32_16x16x32_bf16 v[18:21], v[134:137], v[206:209], v[18:21]
	v_mfma_f32_16x16x32_bf16 v[14:17], v[142:145], v[206:209], v[14:17]
	v_mfma_f32_16x16x32_bf16 v[66:69], v[138:141], v[178:181], v[66:69]
	v_mfma_f32_16x16x32_bf16 v[62:65], v[146:149], v[178:181], v[62:65]
	v_mfma_f32_16x16x32_bf16 v[50:53], v[138:141], v[190:193], v[50:53]
	v_mfma_f32_16x16x32_bf16 v[46:49], v[146:149], v[190:193], v[46:49]
	v_mfma_f32_16x16x32_bf16 v[34:37], v[138:141], v[198:201], v[34:37]
	v_mfma_f32_16x16x32_bf16 v[30:33], v[146:149], v[198:201], v[30:33]
	v_mfma_f32_16x16x32_bf16 v[18:21], v[138:141], v[210:213], v[18:21]
	v_mfma_f32_16x16x32_bf16 v[14:17], v[146:149], v[210:213], v[14:17]
	s_setprio 0
	s_setprio 1
	v_mfma_f32_16x16x32_bf16 v[58:61], v[150:153], v[174:177], v[58:61]
	v_mfma_f32_16x16x32_bf16 v[54:57], v[158:161], v[174:177], v[54:57]
	v_mfma_f32_16x16x32_bf16 v[42:45], v[150:153], v[186:189], v[42:45]
	v_mfma_f32_16x16x32_bf16 v[38:41], v[158:161], v[186:189], v[38:41]
	v_mfma_f32_16x16x32_bf16 v[26:29], v[150:153], v[194:197], v[26:29]
	v_mfma_f32_16x16x32_bf16 v[22:25], v[158:161], v[194:197], v[22:25]
	v_mfma_f32_16x16x32_bf16 v[10:13], v[150:153], v[206:209], v[10:13]
	v_mfma_f32_16x16x32_bf16 v[6:9], v[158:161], v[206:209], v[6:9]
	v_mfma_f32_16x16x32_bf16 v[58:61], v[154:157], v[178:181], v[58:61]
	v_mfma_f32_16x16x32_bf16 v[54:57], v[170:173], v[178:181], v[54:57]
	v_mfma_f32_16x16x32_bf16 v[42:45], v[154:157], v[190:193], v[42:45]
	v_mfma_f32_16x16x32_bf16 v[38:41], v[170:173], v[190:193], v[38:41]
	v_mfma_f32_16x16x32_bf16 v[26:29], v[154:157], v[198:201], v[26:29]
	v_mfma_f32_16x16x32_bf16 v[22:25], v[170:173], v[198:201], v[22:25]
	s_setprio 2
	s_barrier
	v_mfma_f32_16x16x32_bf16 v[10:13], v[154:157], v[210:213], v[10:13]
	v_mfma_f32_16x16x32_bf16 v[6:9], v[170:173], v[210:213], v[6:9]
	s_setprio 0
	s_add_i32 s56, s56, 2
	s_add_u32 s54, s54, 0x100
	s_addc_u32 s55, s55, 0
	s_cmpk_gt_u32 s56, 0x53
	s_mov_b64 s[8:9], s[10:11]
	s_cbranch_scc0 .LBB0_246
	s_branch .Lpeel_x__246

.LBB0_331:
	s_ashr_i32 s15, s14, 31
	s_lshl_b64 s[16:17], s[14:15], 20
	v_readlane_b32 s22, v254, 58
	v_readlane_b32 s23, v254, 59
	s_add_u32 s22, s22, s16
	s_addc_u32 s23, s23, s17
	s_and_b64 s[16:17], s[38:39], exec
	s_cselect_b32 s3, s23, s43
	s_cselect_b32 s15, s22, s42
	s_ashr_i32 s13, s12, 31
	s_lshl_b64 s[16:17], s[12:13], 20
	s_add_u32 s24, s44, s16
	s_addc_u32 s25, s45, s17
	s_and_b64 s[16:17], s[38:39], exec
	s_cselect_b32 s13, s25, s41
	s_cselect_b32 s16, s24, s40
	s_add_u32 s17, s40, 0x100
	s_addc_u32 s67, s41, 0
	s_add_u32 s40, s42, 0x80080
	v_mov_b32_e32 v6, 0
	s_addc_u32 s41, s43, 0
	s_mov_b32 s42, -2
	v_add_u32_e32 v146, s19, v168
	v_add_u32_e32 v166, s48, v168
	ds_read_b128 v[134:137], v146
	ds_read_b128 v[138:141], v146 offset:1024
	ds_read_b128 v[142:145], v146 offset:2048
	ds_read_b128 v[146:149], v146 offset:3072
	ds_read_b128 v[150:153], v166
	ds_read_b128 v[162:165], v166 offset:1024
	ds_read_b128 v[190:193], v166 offset:2048
	ds_read_b128 v[194:197], v166 offset:3072
	s_add_u32 s30, s40, 0xfff80080
	s_addc_u32 s31, s41, -1
	s_cmp_eq_u32 s42, 28
	s_cselect_b32 s31, s3, s31
	s_cselect_b32 s30, s15, s30
	s_cselect_b32 s35, s13, s67
	s_cselect_b32 s34, s16, s17
	v_lshl_add_u64 v[166:167], s[40:41], 0, v[160:161]
	s_add_i32 m0, s51, 0xc000
	ds_read_b128 v[198:201], v187
	ds_read_b128 v[206:209], v187 offset:1024
	ds_read_b128 v[210:213], v187 offset:2048
	ds_read_b128 v[214:217], v187 offset:3072
	ds_read_b128 v[218:221], v187 offset:4096
	ds_read_b128 v[222:225], v187 offset:5120
	ds_read_b128 v[226:229], v187 offset:6144
	ds_read_b128 v[242:245], v187 offset:7168
	global_load_lds_dwordx4 v[166:167], off
	v_lshl_add_u64 v[166:167], s[40:41], 0, v[158:159]
	s_add_i32 m0, s51, 0xe000
	s_nop 0
	global_load_lds_dwordx4 v[166:167], off
	s_waitcnt vmcnt(8)
	s_waitcnt lgkmcnt(0)
	s_barrier
	s_setprio 1
	s_waitcnt lgkmcnt(0)
	v_mfma_f32_16x16x32_bf16 v[130:133], v[134:137], v[198:201], 0
	v_mfma_f32_16x16x32_bf16 v[126:129], v[142:145], v[198:201], 0
	v_mfma_f32_16x16x32_bf16 v[114:117], v[134:137], v[210:213], 0
	v_mfma_f32_16x16x32_bf16 v[110:113], v[142:145], v[210:213], 0
	v_mfma_f32_16x16x32_bf16 v[98:101], v[134:137], v[218:221], 0
	v_mfma_f32_16x16x32_bf16 v[94:97], v[142:145], v[218:221], 0
	v_mfma_f32_16x16x32_bf16 v[82:85], v[134:137], v[226:229], 0
	v_mfma_f32_16x16x32_bf16 v[78:81], v[142:145], v[226:229], 0
	v_mfma_f32_16x16x32_bf16 v[130:133], v[138:141], v[206:209], v[130:133]
	v_mfma_f32_16x16x32_bf16 v[126:129], v[146:149], v[206:209], v[126:129]
	v_mfma_f32_16x16x32_bf16 v[114:117], v[138:141], v[214:217], v[114:117]
	v_mfma_f32_16x16x32_bf16 v[110:113], v[146:149], v[214:217], v[110:113]
	v_mfma_f32_16x16x32_bf16 v[98:101], v[138:141], v[222:225], v[98:101]
	v_mfma_f32_16x16x32_bf16 v[94:97], v[146:149], v[222:225], v[94:97]
	v_mfma_f32_16x16x32_bf16 v[82:85], v[138:141], v[242:245], v[82:85]
	v_mfma_f32_16x16x32_bf16 v[78:81], v[146:149], v[242:245], v[78:81]
	s_setprio 0
	s_setprio 1
	v_mfma_f32_16x16x32_bf16 v[122:125], v[150:153], v[198:201], 0
	v_mfma_f32_16x16x32_bf16 v[118:121], v[190:193], v[198:201], 0
	v_mfma_f32_16x16x32_bf16 v[106:109], v[150:153], v[210:213], 0
	v_mfma_f32_16x16x32_bf16 v[102:105], v[190:193], v[210:213], 0
	v_mfma_f32_16x16x32_bf16 v[90:93], v[150:153], v[218:221], 0
	v_mfma_f32_16x16x32_bf16 v[86:89], v[190:193], v[218:221], 0
	v_mfma_f32_16x16x32_bf16 v[74:77], v[150:153], v[226:229], 0
	v_mfma_f32_16x16x32_bf16 v[70:73], v[190:193], v[226:229], 0
	v_mfma_f32_16x16x32_bf16 v[122:125], v[162:165], v[206:209], v[122:125]
	v_mfma_f32_16x16x32_bf16 v[118:121], v[194:197], v[206:209], v[118:121]
	v_mfma_f32_16x16x32_bf16 v[106:109], v[162:165], v[214:217], v[106:109]
	v_mfma_f32_16x16x32_bf16 v[102:105], v[194:197], v[214:217], v[102:105]
	v_mfma_f32_16x16x32_bf16 v[90:93], v[162:165], v[222:225], v[90:93]
	v_mfma_f32_16x16x32_bf16 v[86:89], v[194:197], v[222:225], v[86:89]
	s_setprio 2
	s_barrier
	v_mfma_f32_16x16x32_bf16 v[74:77], v[162:165], v[242:245], v[74:77]
	v_mfma_f32_16x16x32_bf16 v[70:73], v[194:197], v[242:245], v[70:73]
	s_setprio 0
	s_mov_b32 m0, s46
	v_lshl_add_u64 v[166:167], s[34:35], 0, v[0:1]
	s_add_u32 s68, s34, 0x80000
	ds_read_b128 v[198:201], v187 offset:16384
	ds_read_b128 v[206:209], v187 offset:17408
	ds_read_b128 v[210:213], v187 offset:18432
	ds_read_b128 v[214:217], v187 offset:19456
	ds_read_b128 v[218:221], v187 offset:20480
	ds_read_b128 v[222:225], v187 offset:21504
	ds_read_b128 v[226:229], v187 offset:22528
	ds_read_b128 v[242:245], v187 offset:23552
	global_load_lds_dwordx4 v[166:167], off
	v_lshl_add_u64 v[232:233], s[34:35], 0, v[156:157]
	s_mov_b32 m0, s47
	s_addc_u32 s69, s35, 0
	global_load_lds_dwordx4 v[232:233], off
	v_lshl_add_u64 v[236:237], s[68:69], 0, v[0:1]
	s_mov_b32 m0, s49
	v_lshl_add_u64 v[246:247], s[30:31], 0, v[154:155]
	global_load_lds_dwordx4 v[236:237], off
	v_lshl_add_u64 v[236:237], s[68:69], 0, v[156:157]
	s_mov_b32 m0, s50
	s_nop 0
	global_load_lds_dwordx4 v[236:237], off
	v_lshl_add_u64 v[236:237], s[30:31], 0, v[2:3]
	s_mov_b32 m0, s51
	s_nop 0
	global_load_lds_dwordx4 v[236:237], off
	s_mov_b32 m0, s52
	s_nop 0
	global_load_lds_dwordx4 v[246:247], off
	s_waitcnt vmcnt(8)
	s_waitcnt lgkmcnt(0)
	s_barrier
	s_setprio 1
	s_waitcnt lgkmcnt(0)
	v_mfma_f32_16x16x32_bf16 v[66:69], v[134:137], v[198:201], 0
	v_mfma_f32_16x16x32_bf16 v[62:65], v[142:145], v[198:201], 0
	v_mfma_f32_16x16x32_bf16 v[50:53], v[134:137], v[210:213], 0
	v_mfma_f32_16x16x32_bf16 v[46:49], v[142:145], v[210:213], 0
	v_mfma_f32_16x16x32_bf16 v[34:37], v[134:137], v[218:221], 0
	v_mfma_f32_16x16x32_bf16 v[30:33], v[142:145], v[218:221], 0
	v_mfma_f32_16x16x32_bf16 v[18:21], v[134:137], v[226:229], 0
	v_mfma_f32_16x16x32_bf16 v[14:17], v[142:145], v[226:229], 0
	v_mfma_f32_16x16x32_bf16 v[66:69], v[138:141], v[206:209], v[66:69]
	v_mfma_f32_16x16x32_bf16 v[62:65], v[146:149], v[206:209], v[62:65]
	v_mfma_f32_16x16x32_bf16 v[50:53], v[138:141], v[214:217], v[50:53]
	v_mfma_f32_16x16x32_bf16 v[46:49], v[146:149], v[214:217], v[46:49]
	v_mfma_f32_16x16x32_bf16 v[34:37], v[138:141], v[222:225], v[34:37]
	v_mfma_f32_16x16x32_bf16 v[30:33], v[146:149], v[222:225], v[30:33]
	v_mfma_f32_16x16x32_bf16 v[18:21], v[138:141], v[242:245], v[18:21]
	v_mfma_f32_16x16x32_bf16 v[14:17], v[146:149], v[242:245], v[14:17]
	s_setprio 0
	s_setprio 1
	v_mfma_f32_16x16x32_bf16 v[58:61], v[150:153], v[198:201], 0
	v_mfma_f32_16x16x32_bf16 v[54:57], v[190:193], v[198:201], 0
	v_mfma_f32_16x16x32_bf16 v[42:45], v[150:153], v[210:213], 0
	v_mfma_f32_16x16x32_bf16 v[38:41], v[190:193], v[210:213], 0
	v_mfma_f32_16x16x32_bf16 v[26:29], v[150:153], v[218:221], 0
	v_mfma_f32_16x16x32_bf16 v[22:25], v[190:193], v[218:221], 0
	v_mfma_f32_16x16x32_bf16 v[10:13], v[150:153], v[226:229], 0
	v_mfma_f32_16x16x32_bf16 v[6:9], v[190:193], v[226:229], 0
	v_mfma_f32_16x16x32_bf16 v[58:61], v[162:165], v[206:209], v[58:61]
	v_mfma_f32_16x16x32_bf16 v[54:57], v[194:197], v[206:209], v[54:57]
	v_mfma_f32_16x16x32_bf16 v[42:45], v[162:165], v[214:217], v[42:45]
	v_mfma_f32_16x16x32_bf16 v[38:41], v[194:197], v[214:217], v[38:41]
	v_mfma_f32_16x16x32_bf16 v[26:29], v[162:165], v[222:225], v[26:29]
	v_mfma_f32_16x16x32_bf16 v[22:25], v[194:197], v[222:225], v[22:25]
	s_setprio 2
	s_barrier
	v_mfma_f32_16x16x32_bf16 v[10:13], v[162:165], v[242:245], v[10:13]
	v_mfma_f32_16x16x32_bf16 v[6:9], v[194:197], v[242:245], v[6:9]
	s_setprio 0
	v_add_u32_e32 v146, s56, v168
	v_add_u32_e32 v189, s61, v168
	ds_read_b128 v[134:137], v146
	ds_read_b128 v[138:141], v146 offset:1024
	ds_read_b128 v[142:145], v146 offset:2048
	ds_read_b128 v[146:149], v146 offset:3072
	ds_read_b128 v[150:153], v189
	ds_read_b128 v[162:165], v189 offset:1024
	ds_read_b128 v[190:193], v189 offset:2048
	ds_read_b128 v[194:197], v189 offset:3072
	s_add_u32 s30, s30, 0x80000
	s_addc_u32 s31, s31, 0
	s_mov_b32 m0, s53
	v_lshl_add_u64 v[248:249], s[30:31], 0, v[2:3]
	ds_read_b128 v[198:201], v187 offset:32768
	ds_read_b128 v[206:209], v187 offset:33792
	ds_read_b128 v[210:213], v187 offset:34816
	ds_read_b128 v[214:217], v187 offset:35840
	ds_read_b128 v[218:221], v187 offset:36864
	ds_read_b128 v[222:225], v187 offset:37888
	ds_read_b128 v[226:229], v187 offset:38912
	ds_read_b128 v[242:245], v187 offset:39936
	global_load_lds_dwordx4 v[248:249], off
	v_lshl_add_u64 v[248:249], s[30:31], 0, v[154:155]
	s_mov_b32 m0, s54
	s_nop 0
	global_load_lds_dwordx4 v[248:249], off
	s_waitcnt vmcnt(8)
	s_waitcnt lgkmcnt(0)
	s_barrier
	s_setprio 1
	s_waitcnt lgkmcnt(0)
	v_mfma_f32_16x16x32_bf16 v[130:133], v[134:137], v[198:201], v[130:133]
	v_mfma_f32_16x16x32_bf16 v[126:129], v[142:145], v[198:201], v[126:129]
	v_mfma_f32_16x16x32_bf16 v[114:117], v[134:137], v[210:213], v[114:117]
	v_mfma_f32_16x16x32_bf16 v[110:113], v[142:145], v[210:213], v[110:113]
	v_mfma_f32_16x16x32_bf16 v[98:101], v[134:137], v[218:221], v[98:101]
	v_mfma_f32_16x16x32_bf16 v[94:97], v[142:145], v[218:221], v[94:97]
	v_mfma_f32_16x16x32_bf16 v[82:85], v[134:137], v[226:229], v[82:85]
	v_mfma_f32_16x16x32_bf16 v[78:81], v[142:145], v[226:229], v[78:81]
	v_mfma_f32_16x16x32_bf16 v[130:133], v[138:141], v[206:209], v[130:133]
	v_mfma_f32_16x16x32_bf16 v[126:129], v[146:149], v[206:209], v[126:129]
	v_mfma_f32_16x16x32_bf16 v[114:117], v[138:141], v[214:217], v[114:117]
	v_mfma_f32_16x16x32_bf16 v[110:113], v[146:149], v[214:217], v[110:113]
	v_mfma_f32_16x16x32_bf16 v[98:101], v[138:141], v[222:225], v[98:101]
	v_mfma_f32_16x16x32_bf16 v[94:97], v[146:149], v[222:225], v[94:97]
	v_mfma_f32_16x16x32_bf16 v[82:85], v[138:141], v[242:245], v[82:85]
	v_mfma_f32_16x16x32_bf16 v[78:81], v[146:149], v[242:245], v[78:81]
	s_setprio 0
	s_setprio 1
	v_mfma_f32_16x16x32_bf16 v[122:125], v[150:153], v[198:201], v[122:125]
	v_mfma_f32_16x16x32_bf16 v[118:121], v[190:193], v[198:201], v[118:121]
	v_mfma_f32_16x16x32_bf16 v[106:109], v[150:153], v[210:213], v[106:109]
	v_mfma_f32_16x16x32_bf16 v[102:105], v[190:193], v[210:213], v[102:105]
	v_mfma_f32_16x16x32_bf16 v[90:93], v[150:153], v[218:221], v[90:93]
	v_mfma_f32_16x16x32_bf16 v[86:89], v[190:193], v[218:221], v[86:89]
	v_mfma_f32_16x16x32_bf16 v[74:77], v[150:153], v[226:229], v[74:77]
	v_mfma_f32_16x16x32_bf16 v[70:73], v[190:193], v[226:229], v[70:73]
	v_mfma_f32_16x16x32_bf16 v[122:125], v[162:165], v[206:209], v[122:125]
	v_mfma_f32_16x16x32_bf16 v[118:121], v[194:197], v[206:209], v[118:121]
	v_mfma_f32_16x16x32_bf16 v[106:109], v[162:165], v[214:217], v[106:109]
	v_mfma_f32_16x16x32_bf16 v[102:105], v[194:197], v[214:217], v[102:105]
	v_mfma_f32_16x16x32_bf16 v[90:93], v[162:165], v[222:225], v[90:93]
	v_mfma_f32_16x16x32_bf16 v[86:89], v[194:197], v[222:225], v[86:89]
	s_setprio 2
	s_barrier
	v_mfma_f32_16x16x32_bf16 v[74:77], v[162:165], v[242:245], v[74:77]
	v_mfma_f32_16x16x32_bf16 v[70:73], v[194:197], v[242:245], v[70:73]
	s_setprio 0
	s_mov_b32 m0, s57
	v_lshl_add_u64 v[166:167], v[166:167], 0, s[28:29]
	s_add_u32 s30, s34, 0x80080
	ds_read_b128 v[198:201], v187 offset:49152
	ds_read_b128 v[206:209], v187 offset:50176
	ds_read_b128 v[210:213], v187 offset:51200
	ds_read_b128 v[214:217], v187 offset:52224
	ds_read_b128 v[218:221], v187 offset:53248
	ds_read_b128 v[222:225], v187 offset:54272
	ds_read_b128 v[226:229], v187 offset:55296
	ds_read_b128 v[242:245], v187 offset:56320
	global_load_lds_dwordx4 v[166:167], off
	v_lshl_add_u64 v[166:167], v[232:233], 0, s[28:29]
	s_mov_b32 m0, s58
	s_addc_u32 s31, s35, 0
	global_load_lds_dwordx4 v[166:167], off
	v_lshl_add_u64 v[166:167], s[30:31], 0, v[0:1]
	s_mov_b32 m0, s62
	s_nop 0
	global_load_lds_dwordx4 v[166:167], off
	v_lshl_add_u64 v[166:167], s[30:31], 0, v[156:157]
	s_mov_b32 m0, s63
	s_nop 0
	global_load_lds_dwordx4 v[166:167], off
	v_lshl_add_u64 v[166:167], v[236:237], 0, s[28:29]
	s_mov_b32 m0, s59
	s_nop 0
	global_load_lds_dwordx4 v[166:167], off
	v_lshl_add_u64 v[166:167], v[246:247], 0, s[28:29]
	s_mov_b32 m0, s60
	s_nop 0
	global_load_lds_dwordx4 v[166:167], off
	s_waitcnt vmcnt(8)
	s_waitcnt lgkmcnt(0)
	s_barrier
	s_setprio 1
	s_waitcnt lgkmcnt(0)
	v_mfma_f32_16x16x32_bf16 v[66:69], v[134:137], v[198:201], v[66:69]
	v_mfma_f32_16x16x32_bf16 v[62:65], v[142:145], v[198:201], v[62:65]
	v_mfma_f32_16x16x32_bf16 v[50:53], v[134:137], v[210:213], v[50:53]
	v_mfma_f32_16x16x32_bf16 v[46:49], v[142:145], v[210:213], v[46:49]
	v_mfma_f32_16x16x32_bf16 v[34:37], v[134:137], v[218:221], v[34:37]
	v_mfma_f32_16x16x32_bf16 v[30:33], v[142:145], v[218:221], v[30:33]
	v_mfma_f32_16x16x32_bf16 v[18:21], v[134:137], v[226:229], v[18:21]
	v_mfma_f32_16x16x32_bf16 v[14:17], v[142:145], v[226:229], v[14:17]
	v_mfma_f32_16x16x32_bf16 v[66:69], v[138:141], v[206:209], v[66:69]
	v_mfma_f32_16x16x32_bf16 v[62:65], v[146:149], v[206:209], v[62:65]
	v_mfma_f32_16x16x32_bf16 v[50:53], v[138:141], v[214:217], v[50:53]
	v_mfma_f32_16x16x32_bf16 v[46:49], v[146:149], v[214:217], v[46:49]
	v_mfma_f32_16x16x32_bf16 v[34:37], v[138:141], v[222:225], v[34:37]
	v_mfma_f32_16x16x32_bf16 v[30:33], v[146:149], v[222:225], v[30:33]
	v_mfma_f32_16x16x32_bf16 v[18:21], v[138:141], v[242:245], v[18:21]
	v_mfma_f32_16x16x32_bf16 v[14:17], v[146:149], v[242:245], v[14:17]
	s_setprio 0
	s_setprio 1
	v_mfma_f32_16x16x32_bf16 v[58:61], v[150:153], v[198:201], v[58:61]
	v_mfma_f32_16x16x32_bf16 v[54:57], v[190:193], v[198:201], v[54:57]
	v_mfma_f32_16x16x32_bf16 v[42:45], v[150:153], v[210:213], v[42:45]
	v_mfma_f32_16x16x32_bf16 v[38:41], v[190:193], v[210:213], v[38:41]
	v_mfma_f32_16x16x32_bf16 v[26:29], v[150:153], v[218:221], v[26:29]
	v_mfma_f32_16x16x32_bf16 v[22:25], v[190:193], v[218:221], v[22:25]
	v_mfma_f32_16x16x32_bf16 v[10:13], v[150:153], v[226:229], v[10:13]
	v_mfma_f32_16x16x32_bf16 v[6:9], v[190:193], v[226:229], v[6:9]
	v_mfma_f32_16x16x32_bf16 v[58:61], v[162:165], v[206:209], v[58:61]
	v_mfma_f32_16x16x32_bf16 v[54:57], v[194:197], v[206:209], v[54:57]
	v_mfma_f32_16x16x32_bf16 v[42:45], v[162:165], v[214:217], v[42:45]
	v_mfma_f32_16x16x32_bf16 v[38:41], v[194:197], v[214:217], v[38:41]
	v_mfma_f32_16x16x32_bf16 v[26:29], v[162:165], v[222:225], v[26:29]
	v_mfma_f32_16x16x32_bf16 v[22:25], v[194:197], v[222:225], v[22:25]
	s_setprio 2
	s_barrier
	v_mfma_f32_16x16x32_bf16 v[10:13], v[162:165], v[242:245], v[10:13]
	v_mfma_f32_16x16x32_bf16 v[6:9], v[194:197], v[242:245], v[6:9]
	s_setprio 0
	s_add_i32 s42, s42, 2
	s_add_u32 s17, s17, 0x100
	s_addc_u32 s67, s67, 0
	s_add_u32 s40, s40, 0x100
	s_addc_u32 s41, s41, 0
	s_cmp_gt_u32 s42, 29
	s_cbranch_scc0 .LBB0_332
	s_branch .Lpeel_x__332

.Lpeel_x__332:
	s_and_b64 vcc, exec, s[8:9]
	s_cbranch_vccz .LBB0_335
	s_barrier

.LBB0_1845:
	s_ashr_i32 s11, s10, 31
	s_lshl_b64 s[14:15], s[10:11], 20
	s_add_u32 s14, s20, s14
	s_addc_u32 s15, s30, s15
	s_and_b64 s[2:3], s[2:3], exec
	s_cselect_b32 s11, s15, s23
	s_cselect_b32 s57, s14, s22
	s_add_u32 s58, s22, 0x100
	v_mov_b32_e32 v6, 0
	s_addc_u32 s59, s23, 0
	s_mov_b32 s60, -2
	v_add_u32_e32 v146, s31, v172
	v_add_u32_e32 v170, s38, v172
	ds_read_b128 v[134:137], v146
	ds_read_b128 v[138:141], v146 offset:1024
	ds_read_b128 v[142:145], v146 offset:2048
	ds_read_b128 v[146:149], v146 offset:3072
	ds_read_b128 v[150:153], v170
	ds_read_b128 v[162:165], v170 offset:1024
	ds_read_b128 v[166:169], v170 offset:2048
	ds_read_b128 v[176:179], v170 offset:3072
	s_add_u32 s2, s18, 0x100
	s_addc_u32 s3, s19, 0
	s_cmp_eq_u32 s60, 28
	s_cselect_b32 s25, s13, s3
	s_cselect_b32 s24, s12, s2
	s_cselect_b32 s23, s11, s59
	s_cselect_b32 s22, s57, s58
	v_lshl_add_u64 v[170:171], s[18:19], 0, v[160:161]
	s_add_i32 m0, s41, 0xc000
	ds_read_b128 v[180:183], v174
	ds_read_b128 v[184:187], v174 offset:1024
	ds_read_b128 v[188:191], v174 offset:2048
	ds_read_b128 v[192:195], v174 offset:3072
	ds_read_b128 v[196:199], v174 offset:4096
	ds_read_b128 v[206:209], v174 offset:5120
	ds_read_b128 v[210:213], v174 offset:6144
	ds_read_b128 v[214:217], v174 offset:7168
	global_load_lds_dwordx4 v[170:171], off
	v_lshl_add_u64 v[170:171], s[18:19], 0, v[158:159]
	s_add_i32 m0, s41, 0xe000
	s_nop 0
	global_load_lds_dwordx4 v[170:171], off
	s_waitcnt vmcnt(8)
	s_waitcnt lgkmcnt(0)
	s_barrier
	s_setprio 1
	s_waitcnt lgkmcnt(0)
	v_mfma_f32_16x16x32_bf16 v[130:133], v[134:137], v[180:183], 0
	v_mfma_f32_16x16x32_bf16 v[126:129], v[142:145], v[180:183], 0
	v_mfma_f32_16x16x32_bf16 v[114:117], v[134:137], v[188:191], 0
	v_mfma_f32_16x16x32_bf16 v[110:113], v[142:145], v[188:191], 0
	v_mfma_f32_16x16x32_bf16 v[98:101], v[134:137], v[196:199], 0
	v_mfma_f32_16x16x32_bf16 v[94:97], v[142:145], v[196:199], 0
	v_mfma_f32_16x16x32_bf16 v[82:85], v[134:137], v[210:213], 0
	v_mfma_f32_16x16x32_bf16 v[78:81], v[142:145], v[210:213], 0
	v_mfma_f32_16x16x32_bf16 v[130:133], v[138:141], v[184:187], v[130:133]
	v_mfma_f32_16x16x32_bf16 v[126:129], v[146:149], v[184:187], v[126:129]
	v_mfma_f32_16x16x32_bf16 v[114:117], v[138:141], v[192:195], v[114:117]
	v_mfma_f32_16x16x32_bf16 v[110:113], v[146:149], v[192:195], v[110:113]
	v_mfma_f32_16x16x32_bf16 v[98:101], v[138:141], v[206:209], v[98:101]
	v_mfma_f32_16x16x32_bf16 v[94:97], v[146:149], v[206:209], v[94:97]
	v_mfma_f32_16x16x32_bf16 v[82:85], v[138:141], v[214:217], v[82:85]
	v_mfma_f32_16x16x32_bf16 v[78:81], v[146:149], v[214:217], v[78:81]
	s_setprio 0
	s_setprio 1
	v_mfma_f32_16x16x32_bf16 v[122:125], v[150:153], v[180:183], 0
	v_mfma_f32_16x16x32_bf16 v[118:121], v[166:169], v[180:183], 0
	v_mfma_f32_16x16x32_bf16 v[106:109], v[150:153], v[188:191], 0
	v_mfma_f32_16x16x32_bf16 v[102:105], v[166:169], v[188:191], 0
	v_mfma_f32_16x16x32_bf16 v[90:93], v[150:153], v[196:199], 0
	v_mfma_f32_16x16x32_bf16 v[86:89], v[166:169], v[196:199], 0
	v_mfma_f32_16x16x32_bf16 v[74:77], v[150:153], v[210:213], 0
	v_mfma_f32_16x16x32_bf16 v[70:73], v[166:169], v[210:213], 0
	v_mfma_f32_16x16x32_bf16 v[122:125], v[162:165], v[184:187], v[122:125]
	v_mfma_f32_16x16x32_bf16 v[118:121], v[176:179], v[184:187], v[118:121]
	v_mfma_f32_16x16x32_bf16 v[106:109], v[162:165], v[192:195], v[106:109]
	v_mfma_f32_16x16x32_bf16 v[102:105], v[176:179], v[192:195], v[102:105]
	v_mfma_f32_16x16x32_bf16 v[90:93], v[162:165], v[206:209], v[90:93]
	v_mfma_f32_16x16x32_bf16 v[86:89], v[176:179], v[206:209], v[86:89]
	s_setprio 2
	s_barrier
	v_mfma_f32_16x16x32_bf16 v[74:77], v[162:165], v[214:217], v[74:77]
	v_mfma_f32_16x16x32_bf16 v[70:73], v[176:179], v[214:217], v[70:73]
	s_setprio 0
	s_mov_b32 m0, s34
	v_lshl_add_u64 v[170:171], s[22:23], 0, v[0:1]
	s_add_u32 s18, s22, 0x80000
	ds_read_b128 v[180:183], v174 offset:16384
	ds_read_b128 v[184:187], v174 offset:17408
	ds_read_b128 v[188:191], v174 offset:18432
	ds_read_b128 v[192:195], v174 offset:19456
	ds_read_b128 v[196:199], v174 offset:20480
	ds_read_b128 v[206:209], v174 offset:21504
	ds_read_b128 v[210:213], v174 offset:22528
	ds_read_b128 v[214:217], v174 offset:23552
	global_load_lds_dwordx4 v[170:171], off
	v_lshl_add_u64 v[200:201], s[22:23], 0, v[156:157]
	s_mov_b32 m0, s35
	s_addc_u32 s19, s23, 0
	global_load_lds_dwordx4 v[200:201], off
	v_lshl_add_u64 v[218:219], s[18:19], 0, v[0:1]
	s_mov_b32 m0, s39
	v_lshl_add_u64 v[220:221], s[24:25], 0, v[154:155]
	global_load_lds_dwordx4 v[218:219], off
	v_lshl_add_u64 v[218:219], s[18:19], 0, v[156:157]
	s_mov_b32 m0, s40
	s_nop 0
	global_load_lds_dwordx4 v[218:219], off
	v_lshl_add_u64 v[218:219], s[24:25], 0, v[2:3]
	s_mov_b32 m0, s41
	s_nop 0
	global_load_lds_dwordx4 v[218:219], off
	s_mov_b32 m0, s42
	s_nop 0
	global_load_lds_dwordx4 v[220:221], off
	s_waitcnt vmcnt(8)
	s_waitcnt lgkmcnt(0)
	s_barrier
	s_setprio 1
	s_waitcnt lgkmcnt(0)
	v_mfma_f32_16x16x32_bf16 v[66:69], v[134:137], v[180:183], 0
	v_mfma_f32_16x16x32_bf16 v[62:65], v[142:145], v[180:183], 0
	v_mfma_f32_16x16x32_bf16 v[50:53], v[134:137], v[188:191], 0
	v_mfma_f32_16x16x32_bf16 v[46:49], v[142:145], v[188:191], 0
	v_mfma_f32_16x16x32_bf16 v[34:37], v[134:137], v[196:199], 0
	v_mfma_f32_16x16x32_bf16 v[30:33], v[142:145], v[196:199], 0
	v_mfma_f32_16x16x32_bf16 v[18:21], v[134:137], v[210:213], 0
	v_mfma_f32_16x16x32_bf16 v[14:17], v[142:145], v[210:213], 0
	v_mfma_f32_16x16x32_bf16 v[66:69], v[138:141], v[184:187], v[66:69]
	v_mfma_f32_16x16x32_bf16 v[62:65], v[146:149], v[184:187], v[62:65]
	v_mfma_f32_16x16x32_bf16 v[50:53], v[138:141], v[192:195], v[50:53]
	v_mfma_f32_16x16x32_bf16 v[46:49], v[146:149], v[192:195], v[46:49]
	v_mfma_f32_16x16x32_bf16 v[34:37], v[138:141], v[206:209], v[34:37]
	v_mfma_f32_16x16x32_bf16 v[30:33], v[146:149], v[206:209], v[30:33]
	v_mfma_f32_16x16x32_bf16 v[18:21], v[138:141], v[214:217], v[18:21]
	v_mfma_f32_16x16x32_bf16 v[14:17], v[146:149], v[214:217], v[14:17]
	s_setprio 0
	s_setprio 1
	v_mfma_f32_16x16x32_bf16 v[58:61], v[150:153], v[180:183], 0
	v_mfma_f32_16x16x32_bf16 v[54:57], v[166:169], v[180:183], 0
	v_mfma_f32_16x16x32_bf16 v[42:45], v[150:153], v[188:191], 0
	v_mfma_f32_16x16x32_bf16 v[38:41], v[166:169], v[188:191], 0
	v_mfma_f32_16x16x32_bf16 v[26:29], v[150:153], v[196:199], 0
	v_mfma_f32_16x16x32_bf16 v[22:25], v[166:169], v[196:199], 0
	v_mfma_f32_16x16x32_bf16 v[10:13], v[150:153], v[210:213], 0
	v_mfma_f32_16x16x32_bf16 v[6:9], v[166:169], v[210:213], 0
	v_mfma_f32_16x16x32_bf16 v[58:61], v[162:165], v[184:187], v[58:61]
	v_mfma_f32_16x16x32_bf16 v[54:57], v[176:179], v[184:187], v[54:57]
	v_mfma_f32_16x16x32_bf16 v[42:45], v[162:165], v[192:195], v[42:45]
	v_mfma_f32_16x16x32_bf16 v[38:41], v[176:179], v[192:195], v[38:41]
	v_mfma_f32_16x16x32_bf16 v[26:29], v[162:165], v[206:209], v[26:29]
	v_mfma_f32_16x16x32_bf16 v[22:25], v[176:179], v[206:209], v[22:25]
	s_setprio 2
	s_barrier
	v_mfma_f32_16x16x32_bf16 v[10:13], v[162:165], v[214:217], v[10:13]
	v_mfma_f32_16x16x32_bf16 v[6:9], v[176:179], v[214:217], v[6:9]
	s_setprio 0
	v_add_u32_e32 v146, s45, v172
	v_add_u32_e32 v175, s50, v172
	ds_read_b128 v[134:137], v146
	ds_read_b128 v[138:141], v146 offset:1024
	ds_read_b128 v[142:145], v146 offset:2048
	ds_read_b128 v[146:149], v146 offset:3072
	ds_read_b128 v[150:153], v175
	ds_read_b128 v[162:165], v175 offset:1024
	ds_read_b128 v[166:169], v175 offset:2048
	ds_read_b128 v[176:179], v175 offset:3072
	s_add_u32 s18, s24, 0x280000
	s_addc_u32 s19, s25, 0
	s_mov_b32 m0, s43
	v_lshl_add_u64 v[222:223], s[18:19], 0, v[2:3]
	ds_read_b128 v[180:183], v174 offset:32768
	ds_read_b128 v[184:187], v174 offset:33792
	ds_read_b128 v[188:191], v174 offset:34816
	ds_read_b128 v[192:195], v174 offset:35840
	ds_read_b128 v[196:199], v174 offset:36864
	ds_read_b128 v[206:209], v174 offset:37888
	ds_read_b128 v[210:213], v174 offset:38912
	ds_read_b128 v[214:217], v174 offset:39936
	global_load_lds_dwordx4 v[222:223], off
	v_lshl_add_u64 v[222:223], s[18:19], 0, v[154:155]
	s_mov_b32 m0, s44
	s_nop 0
	global_load_lds_dwordx4 v[222:223], off
	s_waitcnt vmcnt(8)
	s_waitcnt lgkmcnt(0)
	s_barrier
	s_setprio 1
	s_waitcnt lgkmcnt(0)
	v_mfma_f32_16x16x32_bf16 v[130:133], v[134:137], v[180:183], v[130:133]
	v_mfma_f32_16x16x32_bf16 v[126:129], v[142:145], v[180:183], v[126:129]
	v_mfma_f32_16x16x32_bf16 v[114:117], v[134:137], v[188:191], v[114:117]
	v_mfma_f32_16x16x32_bf16 v[110:113], v[142:145], v[188:191], v[110:113]
	v_mfma_f32_16x16x32_bf16 v[98:101], v[134:137], v[196:199], v[98:101]
	v_mfma_f32_16x16x32_bf16 v[94:97], v[142:145], v[196:199], v[94:97]
	v_mfma_f32_16x16x32_bf16 v[82:85], v[134:137], v[210:213], v[82:85]
	v_mfma_f32_16x16x32_bf16 v[78:81], v[142:145], v[210:213], v[78:81]
	v_mfma_f32_16x16x32_bf16 v[130:133], v[138:141], v[184:187], v[130:133]
	v_mfma_f32_16x16x32_bf16 v[126:129], v[146:149], v[184:187], v[126:129]
	v_mfma_f32_16x16x32_bf16 v[114:117], v[138:141], v[192:195], v[114:117]
	v_mfma_f32_16x16x32_bf16 v[110:113], v[146:149], v[192:195], v[110:113]
	v_mfma_f32_16x16x32_bf16 v[98:101], v[138:141], v[206:209], v[98:101]
	v_mfma_f32_16x16x32_bf16 v[94:97], v[146:149], v[206:209], v[94:97]
	v_mfma_f32_16x16x32_bf16 v[82:85], v[138:141], v[214:217], v[82:85]
	v_mfma_f32_16x16x32_bf16 v[78:81], v[146:149], v[214:217], v[78:81]
	s_setprio 0
	s_setprio 1
	v_mfma_f32_16x16x32_bf16 v[122:125], v[150:153], v[180:183], v[122:125]
	v_mfma_f32_16x16x32_bf16 v[118:121], v[166:169], v[180:183], v[118:121]
	v_mfma_f32_16x16x32_bf16 v[106:109], v[150:153], v[188:191], v[106:109]
	v_mfma_f32_16x16x32_bf16 v[102:105], v[166:169], v[188:191], v[102:105]
	v_mfma_f32_16x16x32_bf16 v[90:93], v[150:153], v[196:199], v[90:93]
	v_mfma_f32_16x16x32_bf16 v[86:89], v[166:169], v[196:199], v[86:89]
	v_mfma_f32_16x16x32_bf16 v[74:77], v[150:153], v[210:213], v[74:77]
	v_mfma_f32_16x16x32_bf16 v[70:73], v[166:169], v[210:213], v[70:73]
	v_mfma_f32_16x16x32_bf16 v[122:125], v[162:165], v[184:187], v[122:125]
	v_mfma_f32_16x16x32_bf16 v[118:121], v[176:179], v[184:187], v[118:121]
	v_mfma_f32_16x16x32_bf16 v[106:109], v[162:165], v[192:195], v[106:109]
	v_mfma_f32_16x16x32_bf16 v[102:105], v[176:179], v[192:195], v[102:105]
	v_mfma_f32_16x16x32_bf16 v[90:93], v[162:165], v[206:209], v[90:93]
	v_mfma_f32_16x16x32_bf16 v[86:89], v[176:179], v[206:209], v[86:89]
	s_setprio 2
	s_barrier
	v_mfma_f32_16x16x32_bf16 v[74:77], v[162:165], v[214:217], v[74:77]
	v_mfma_f32_16x16x32_bf16 v[70:73], v[176:179], v[214:217], v[70:73]
	s_setprio 0
	s_mov_b32 m0, s46
	v_lshl_add_u64 v[170:171], v[170:171], 0, s[28:29]
	s_add_u32 s18, s22, 0x80080
	ds_read_b128 v[180:183], v174 offset:49152
	ds_read_b128 v[184:187], v174 offset:50176
	ds_read_b128 v[188:191], v174 offset:51200
	ds_read_b128 v[192:195], v174 offset:52224
	ds_read_b128 v[196:199], v174 offset:53248
	ds_read_b128 v[206:209], v174 offset:54272
	ds_read_b128 v[210:213], v174 offset:55296
	ds_read_b128 v[214:217], v174 offset:56320
	global_load_lds_dwordx4 v[170:171], off
	v_lshl_add_u64 v[170:171], v[200:201], 0, s[28:29]
	s_mov_b32 m0, s47
	s_addc_u32 s19, s23, 0
	global_load_lds_dwordx4 v[170:171], off
	v_lshl_add_u64 v[170:171], s[18:19], 0, v[0:1]
	s_mov_b32 m0, s51
	s_nop 0
	global_load_lds_dwordx4 v[170:171], off
	v_lshl_add_u64 v[170:171], s[18:19], 0, v[156:157]
	s_mov_b32 m0, s52
	s_nop 0
	global_load_lds_dwordx4 v[170:171], off
	v_lshl_add_u64 v[170:171], v[218:219], 0, s[28:29]
	s_mov_b32 m0, s48
	s_nop 0
	global_load_lds_dwordx4 v[170:171], off
	v_lshl_add_u64 v[170:171], v[220:221], 0, s[28:29]
	s_mov_b32 m0, s49
	s_nop 0
	global_load_lds_dwordx4 v[170:171], off
	s_waitcnt vmcnt(8)
	s_waitcnt lgkmcnt(0)
	s_barrier
	s_setprio 1
	s_waitcnt lgkmcnt(0)
	v_mfma_f32_16x16x32_bf16 v[66:69], v[134:137], v[180:183], v[66:69]
	v_mfma_f32_16x16x32_bf16 v[62:65], v[142:145], v[180:183], v[62:65]
	v_mfma_f32_16x16x32_bf16 v[50:53], v[134:137], v[188:191], v[50:53]
	v_mfma_f32_16x16x32_bf16 v[46:49], v[142:145], v[188:191], v[46:49]
	v_mfma_f32_16x16x32_bf16 v[34:37], v[134:137], v[196:199], v[34:37]
	v_mfma_f32_16x16x32_bf16 v[30:33], v[142:145], v[196:199], v[30:33]
	v_mfma_f32_16x16x32_bf16 v[18:21], v[134:137], v[210:213], v[18:21]
	v_mfma_f32_16x16x32_bf16 v[14:17], v[142:145], v[210:213], v[14:17]
	v_mfma_f32_16x16x32_bf16 v[66:69], v[138:141], v[184:187], v[66:69]
	v_mfma_f32_16x16x32_bf16 v[62:65], v[146:149], v[184:187], v[62:65]
	v_mfma_f32_16x16x32_bf16 v[50:53], v[138:141], v[192:195], v[50:53]
	v_mfma_f32_16x16x32_bf16 v[46:49], v[146:149], v[192:195], v[46:49]
	v_mfma_f32_16x16x32_bf16 v[34:37], v[138:141], v[206:209], v[34:37]
	v_mfma_f32_16x16x32_bf16 v[30:33], v[146:149], v[206:209], v[30:33]
	v_mfma_f32_16x16x32_bf16 v[18:21], v[138:141], v[214:217], v[18:21]
	v_mfma_f32_16x16x32_bf16 v[14:17], v[146:149], v[214:217], v[14:17]
	s_setprio 0
	s_setprio 1
	v_mfma_f32_16x16x32_bf16 v[58:61], v[150:153], v[180:183], v[58:61]
	v_mfma_f32_16x16x32_bf16 v[54:57], v[166:169], v[180:183], v[54:57]
	v_mfma_f32_16x16x32_bf16 v[42:45], v[150:153], v[188:191], v[42:45]
	v_mfma_f32_16x16x32_bf16 v[38:41], v[166:169], v[188:191], v[38:41]
	v_mfma_f32_16x16x32_bf16 v[26:29], v[150:153], v[196:199], v[26:29]
	v_mfma_f32_16x16x32_bf16 v[22:25], v[166:169], v[196:199], v[22:25]
	v_mfma_f32_16x16x32_bf16 v[10:13], v[150:153], v[210:213], v[10:13]
	v_mfma_f32_16x16x32_bf16 v[6:9], v[166:169], v[210:213], v[6:9]
	v_mfma_f32_16x16x32_bf16 v[58:61], v[162:165], v[184:187], v[58:61]
	v_mfma_f32_16x16x32_bf16 v[54:57], v[176:179], v[184:187], v[54:57]
	v_mfma_f32_16x16x32_bf16 v[42:45], v[162:165], v[192:195], v[42:45]
	v_mfma_f32_16x16x32_bf16 v[38:41], v[176:179], v[192:195], v[38:41]
	v_mfma_f32_16x16x32_bf16 v[26:29], v[162:165], v[206:209], v[26:29]
	v_mfma_f32_16x16x32_bf16 v[22:25], v[176:179], v[206:209], v[22:25]
	s_setprio 2
	s_barrier
	v_mfma_f32_16x16x32_bf16 v[10:13], v[162:165], v[214:217], v[10:13]
	v_mfma_f32_16x16x32_bf16 v[6:9], v[176:179], v[214:217], v[6:9]
	s_setprio 0
	s_add_i32 s60, s60, 2
	s_add_u32 s58, s58, 0x100
	s_addc_u32 s59, s59, 0
	s_cmp_gt_u32 s60, 29
	s_mov_b64 s[18:19], s[2:3]
	s_cbranch_scc0 .LBB0_1846
	s_branch .Lpeel_x__1846

.LBB0_1874:
	s_ashr_i32 s13, s12, 31
	s_lshl_b64 s[14:15], s[12:13], 19
	s_add_u32 s14, s21, s14
	s_addc_u32 s15, s26, s15
	s_and_b64 s[16:17], s[36:37], exec
	s_cselect_b32 s13, s15, s23
	s_cselect_b32 s56, s14, s22
	s_ashr_i32 s11, s10, 31
	s_lshl_b64 s[16:17], s[10:11], 19
	s_add_u32 s16, s31, s16
	s_addc_u32 s17, s34, s17
	s_and_b64 s[24:25], s[36:37], exec
	s_cselect_b32 s11, s17, s19
	s_cselect_b32 s57, s16, s18
	s_add_u32 s58, s18, 0x100
	s_addc_u32 s59, s19, 0
	s_add_u32 s18, s22, 0x40080
	v_mov_b32_e32 v6, 0
	s_addc_u32 s19, s23, 0
	s_mov_b32 s60, -2
	v_add_u32_e32 v138, s35, v241
	v_add_u32_e32 v162, s40, v241
	ds_read_b128 v[118:121], v138
	ds_read_b128 v[122:125], v138 offset:1024
	ds_read_b128 v[130:133], v138 offset:2048
	ds_read_b128 v[138:141], v138 offset:3072
	ds_read_b128 v[142:145], v162
	ds_read_b128 v[150:153], v162 offset:1024
	ds_read_b128 v[154:157], v162 offset:2048
	ds_read_b128 v[162:165], v162 offset:3072
	s_add_u32 s22, s18, 0xfffc0080
	s_addc_u32 s23, s19, -1
	s_cmp_eq_u32 s60, 12
	s_cselect_b32 s25, s13, s23
	s_cselect_b32 s24, s56, s22
	s_cselect_b32 s23, s11, s59
	s_cselect_b32 s22, s57, s58
	v_lshl_add_u64 v[198:199], s[18:19], 0, v[212:213]
	s_add_i32 m0, s43, 0xc000
	ds_read_b128 v[166:169], v243
	ds_read_b128 v[170:173], v243 offset:1024
	ds_read_b128 v[174:177], v243 offset:2048
	ds_read_b128 v[178:181], v243 offset:3072
	ds_read_b128 v[182:185], v243 offset:4096
	ds_read_b128 v[186:189], v243 offset:5120
	ds_read_b128 v[190:193], v243 offset:6144
	ds_read_b128 v[194:197], v243 offset:7168
	global_load_lds_dwordx4 v[198:199], off
	v_lshl_add_u64 v[198:199], s[18:19], 0, v[210:211]
	s_add_i32 m0, s43, 0xe000
	s_nop 0
	global_load_lds_dwordx4 v[198:199], off
	s_waitcnt vmcnt(8)
	s_waitcnt lgkmcnt(0)
	s_barrier
	s_setprio 1
	s_waitcnt lgkmcnt(0)
	v_mfma_f32_16x16x32_bf16 v[158:161], v[118:121], v[166:169], 0
	v_mfma_f32_16x16x32_bf16 v[146:149], v[130:133], v[166:169], 0
	v_mfma_f32_16x16x32_bf16 v[114:117], v[118:121], v[174:177], 0
	v_mfma_f32_16x16x32_bf16 v[110:113], v[130:133], v[174:177], 0
	v_mfma_f32_16x16x32_bf16 v[98:101], v[118:121], v[182:185], 0
	v_mfma_f32_16x16x32_bf16 v[94:97], v[130:133], v[182:185], 0
	v_mfma_f32_16x16x32_bf16 v[82:85], v[118:121], v[190:193], 0
	v_mfma_f32_16x16x32_bf16 v[78:81], v[130:133], v[190:193], 0
	v_mfma_f32_16x16x32_bf16 v[158:161], v[122:125], v[170:173], v[158:161]
	v_mfma_f32_16x16x32_bf16 v[146:149], v[138:141], v[170:173], v[146:149]
	v_mfma_f32_16x16x32_bf16 v[114:117], v[122:125], v[178:181], v[114:117]
	v_mfma_f32_16x16x32_bf16 v[110:113], v[138:141], v[178:181], v[110:113]
	v_mfma_f32_16x16x32_bf16 v[98:101], v[122:125], v[186:189], v[98:101]
	v_mfma_f32_16x16x32_bf16 v[94:97], v[138:141], v[186:189], v[94:97]
	v_mfma_f32_16x16x32_bf16 v[82:85], v[122:125], v[194:197], v[82:85]
	v_mfma_f32_16x16x32_bf16 v[78:81], v[138:141], v[194:197], v[78:81]
	s_setprio 0
	s_setprio 1
	v_mfma_f32_16x16x32_bf16 v[134:137], v[142:145], v[166:169], 0
	v_mfma_f32_16x16x32_bf16 v[126:129], v[154:157], v[166:169], 0
	v_mfma_f32_16x16x32_bf16 v[106:109], v[142:145], v[174:177], 0
	v_mfma_f32_16x16x32_bf16 v[102:105], v[154:157], v[174:177], 0
	v_mfma_f32_16x16x32_bf16 v[90:93], v[142:145], v[182:185], 0
	v_mfma_f32_16x16x32_bf16 v[86:89], v[154:157], v[182:185], 0
	v_mfma_f32_16x16x32_bf16 v[74:77], v[142:145], v[190:193], 0
	v_mfma_f32_16x16x32_bf16 v[70:73], v[154:157], v[190:193], 0
	v_mfma_f32_16x16x32_bf16 v[134:137], v[150:153], v[170:173], v[134:137]
	v_mfma_f32_16x16x32_bf16 v[126:129], v[162:165], v[170:173], v[126:129]
	v_mfma_f32_16x16x32_bf16 v[106:109], v[150:153], v[178:181], v[106:109]
	v_mfma_f32_16x16x32_bf16 v[102:105], v[162:165], v[178:181], v[102:105]
	v_mfma_f32_16x16x32_bf16 v[90:93], v[150:153], v[186:189], v[90:93]
	v_mfma_f32_16x16x32_bf16 v[86:89], v[162:165], v[186:189], v[86:89]
	s_setprio 2
	s_barrier
	v_mfma_f32_16x16x32_bf16 v[74:77], v[150:153], v[194:197], v[74:77]
	v_mfma_f32_16x16x32_bf16 v[70:73], v[162:165], v[194:197], v[70:73]
	s_setprio 0
	s_mov_b32 m0, s38
	v_lshl_add_u64 v[198:199], s[22:23], 0, v[0:1]
	s_add_u32 s62, s22, 0x40000
	ds_read_b128 v[166:169], v243 offset:16384
	ds_read_b128 v[170:173], v243 offset:17408
	ds_read_b128 v[174:177], v243 offset:18432
	ds_read_b128 v[178:181], v243 offset:19456
	ds_read_b128 v[182:185], v243 offset:20480
	ds_read_b128 v[186:189], v243 offset:21504
	ds_read_b128 v[190:193], v243 offset:22528
	ds_read_b128 v[194:197], v243 offset:23552
	global_load_lds_dwordx4 v[198:199], off
	v_lshl_add_u64 v[200:201], s[22:23], 0, v[208:209]
	s_mov_b32 m0, s39
	s_addc_u32 s63, s23, 0
	global_load_lds_dwordx4 v[200:201], off
	v_lshl_add_u64 v[214:215], s[62:63], 0, v[0:1]
	s_mov_b32 m0, s41
	v_lshl_add_u64 v[216:217], s[24:25], 0, v[206:207]
	global_load_lds_dwordx4 v[214:215], off
	v_lshl_add_u64 v[214:215], s[62:63], 0, v[208:209]
	s_mov_b32 m0, s42
	s_nop 0
	global_load_lds_dwordx4 v[214:215], off
	v_lshl_add_u64 v[214:215], s[24:25], 0, v[2:3]
	s_mov_b32 m0, s43
	s_nop 0
	global_load_lds_dwordx4 v[214:215], off
	s_mov_b32 m0, s44
	s_nop 0
	global_load_lds_dwordx4 v[216:217], off
	s_waitcnt vmcnt(8)
	s_waitcnt lgkmcnt(0)
	s_barrier
	s_setprio 1
	s_waitcnt lgkmcnt(0)
	v_mfma_f32_16x16x32_bf16 v[66:69], v[118:121], v[166:169], 0
	v_mfma_f32_16x16x32_bf16 v[62:65], v[130:133], v[166:169], 0
	v_mfma_f32_16x16x32_bf16 v[50:53], v[118:121], v[174:177], 0
	v_mfma_f32_16x16x32_bf16 v[46:49], v[130:133], v[174:177], 0
	v_mfma_f32_16x16x32_bf16 v[34:37], v[118:121], v[182:185], 0
	v_mfma_f32_16x16x32_bf16 v[30:33], v[130:133], v[182:185], 0
	v_mfma_f32_16x16x32_bf16 v[18:21], v[118:121], v[190:193], 0
	v_mfma_f32_16x16x32_bf16 v[14:17], v[130:133], v[190:193], 0
	v_mfma_f32_16x16x32_bf16 v[66:69], v[122:125], v[170:173], v[66:69]
	v_mfma_f32_16x16x32_bf16 v[62:65], v[138:141], v[170:173], v[62:65]
	v_mfma_f32_16x16x32_bf16 v[50:53], v[122:125], v[178:181], v[50:53]
	v_mfma_f32_16x16x32_bf16 v[46:49], v[138:141], v[178:181], v[46:49]
	v_mfma_f32_16x16x32_bf16 v[34:37], v[122:125], v[186:189], v[34:37]
	v_mfma_f32_16x16x32_bf16 v[30:33], v[138:141], v[186:189], v[30:33]
	v_mfma_f32_16x16x32_bf16 v[18:21], v[122:125], v[194:197], v[18:21]
	v_mfma_f32_16x16x32_bf16 v[14:17], v[138:141], v[194:197], v[14:17]
	s_setprio 0
	s_setprio 1
	v_mfma_f32_16x16x32_bf16 v[58:61], v[142:145], v[166:169], 0
	v_mfma_f32_16x16x32_bf16 v[54:57], v[154:157], v[166:169], 0
	v_mfma_f32_16x16x32_bf16 v[42:45], v[142:145], v[174:177], 0
	v_mfma_f32_16x16x32_bf16 v[38:41], v[154:157], v[174:177], 0
	v_mfma_f32_16x16x32_bf16 v[26:29], v[142:145], v[182:185], 0
	v_mfma_f32_16x16x32_bf16 v[22:25], v[154:157], v[182:185], 0
	v_mfma_f32_16x16x32_bf16 v[10:13], v[142:145], v[190:193], 0
	v_mfma_f32_16x16x32_bf16 v[6:9], v[154:157], v[190:193], 0
	v_mfma_f32_16x16x32_bf16 v[58:61], v[150:153], v[170:173], v[58:61]
	v_mfma_f32_16x16x32_bf16 v[54:57], v[162:165], v[170:173], v[54:57]
	v_mfma_f32_16x16x32_bf16 v[42:45], v[150:153], v[178:181], v[42:45]
	v_mfma_f32_16x16x32_bf16 v[38:41], v[162:165], v[178:181], v[38:41]
	v_mfma_f32_16x16x32_bf16 v[26:29], v[150:153], v[186:189], v[26:29]
	v_mfma_f32_16x16x32_bf16 v[22:25], v[162:165], v[186:189], v[22:25]
	s_setprio 2
	s_barrier
	v_mfma_f32_16x16x32_bf16 v[10:13], v[150:153], v[194:197], v[10:13]
	v_mfma_f32_16x16x32_bf16 v[6:9], v[162:165], v[194:197], v[6:9]
	s_setprio 0
	v_add_u32_e32 v138, s47, v241
	v_add_u32_e32 v162, s52, v241
	ds_read_b128 v[118:121], v138
	ds_read_b128 v[122:125], v138 offset:1024
	ds_read_b128 v[130:133], v138 offset:2048
	ds_read_b128 v[138:141], v138 offset:3072
	ds_read_b128 v[142:145], v162
	ds_read_b128 v[150:153], v162 offset:1024
	ds_read_b128 v[154:157], v162 offset:2048
	ds_read_b128 v[162:165], v162 offset:3072
	s_add_u32 s24, s24, 0x40000
	s_addc_u32 s25, s25, 0
	s_mov_b32 m0, s45
	v_lshl_add_u64 v[218:219], s[24:25], 0, v[2:3]
	ds_read_b128 v[166:169], v243 offset:32768
	ds_read_b128 v[170:173], v243 offset:33792
	ds_read_b128 v[174:177], v243 offset:34816
	ds_read_b128 v[178:181], v243 offset:35840
	ds_read_b128 v[182:185], v243 offset:36864
	ds_read_b128 v[186:189], v243 offset:37888
	ds_read_b128 v[190:193], v243 offset:38912
	ds_read_b128 v[194:197], v243 offset:39936
	global_load_lds_dwordx4 v[218:219], off
	v_lshl_add_u64 v[218:219], s[24:25], 0, v[206:207]
	s_mov_b32 m0, s46
	s_nop 0
	global_load_lds_dwordx4 v[218:219], off
	s_waitcnt vmcnt(8)
	s_waitcnt lgkmcnt(0)
	s_barrier
	s_setprio 1
	s_waitcnt lgkmcnt(0)
	v_mfma_f32_16x16x32_bf16 v[158:161], v[118:121], v[166:169], v[158:161]
	v_mfma_f32_16x16x32_bf16 v[146:149], v[130:133], v[166:169], v[146:149]
	v_mfma_f32_16x16x32_bf16 v[114:117], v[118:121], v[174:177], v[114:117]
	v_mfma_f32_16x16x32_bf16 v[110:113], v[130:133], v[174:177], v[110:113]
	v_mfma_f32_16x16x32_bf16 v[98:101], v[118:121], v[182:185], v[98:101]
	v_mfma_f32_16x16x32_bf16 v[94:97], v[130:133], v[182:185], v[94:97]
	v_mfma_f32_16x16x32_bf16 v[82:85], v[118:121], v[190:193], v[82:85]
	v_mfma_f32_16x16x32_bf16 v[78:81], v[130:133], v[190:193], v[78:81]
	v_mfma_f32_16x16x32_bf16 v[158:161], v[122:125], v[170:173], v[158:161]
	v_mfma_f32_16x16x32_bf16 v[146:149], v[138:141], v[170:173], v[146:149]
	v_mfma_f32_16x16x32_bf16 v[114:117], v[122:125], v[178:181], v[114:117]
	v_mfma_f32_16x16x32_bf16 v[110:113], v[138:141], v[178:181], v[110:113]
	v_mfma_f32_16x16x32_bf16 v[98:101], v[122:125], v[186:189], v[98:101]
	v_mfma_f32_16x16x32_bf16 v[94:97], v[138:141], v[186:189], v[94:97]
	v_mfma_f32_16x16x32_bf16 v[82:85], v[122:125], v[194:197], v[82:85]
	v_mfma_f32_16x16x32_bf16 v[78:81], v[138:141], v[194:197], v[78:81]
	s_setprio 0
	s_setprio 1
	v_mfma_f32_16x16x32_bf16 v[134:137], v[142:145], v[166:169], v[134:137]
	v_mfma_f32_16x16x32_bf16 v[126:129], v[154:157], v[166:169], v[126:129]
	v_mfma_f32_16x16x32_bf16 v[106:109], v[142:145], v[174:177], v[106:109]
	v_mfma_f32_16x16x32_bf16 v[102:105], v[154:157], v[174:177], v[102:105]
	v_mfma_f32_16x16x32_bf16 v[90:93], v[142:145], v[182:185], v[90:93]
	v_mfma_f32_16x16x32_bf16 v[86:89], v[154:157], v[182:185], v[86:89]
	v_mfma_f32_16x16x32_bf16 v[74:77], v[142:145], v[190:193], v[74:77]
	v_mfma_f32_16x16x32_bf16 v[70:73], v[154:157], v[190:193], v[70:73]
	v_mfma_f32_16x16x32_bf16 v[134:137], v[150:153], v[170:173], v[134:137]
	v_mfma_f32_16x16x32_bf16 v[126:129], v[162:165], v[170:173], v[126:129]
	v_mfma_f32_16x16x32_bf16 v[106:109], v[150:153], v[178:181], v[106:109]
	v_mfma_f32_16x16x32_bf16 v[102:105], v[162:165], v[178:181], v[102:105]
	v_mfma_f32_16x16x32_bf16 v[90:93], v[150:153], v[186:189], v[90:93]
	v_mfma_f32_16x16x32_bf16 v[86:89], v[162:165], v[186:189], v[86:89]
	s_setprio 2
	s_barrier
	v_mfma_f32_16x16x32_bf16 v[74:77], v[150:153], v[194:197], v[74:77]
	v_mfma_f32_16x16x32_bf16 v[70:73], v[162:165], v[194:197], v[70:73]
	s_setprio 0
	s_mov_b32 m0, s48
	v_lshl_add_u64 v[198:199], v[198:199], 0, s[28:29]
	s_add_u32 s22, s22, 0x40080
	ds_read_b128 v[166:169], v243 offset:49152
	ds_read_b128 v[170:173], v243 offset:50176
	ds_read_b128 v[174:177], v243 offset:51200
	ds_read_b128 v[178:181], v243 offset:52224
	ds_read_b128 v[182:185], v243 offset:53248
	ds_read_b128 v[186:189], v243 offset:54272
	ds_read_b128 v[190:193], v243 offset:55296
	ds_read_b128 v[194:197], v243 offset:56320
	global_load_lds_dwordx4 v[198:199], off
	v_lshl_add_u64 v[198:199], v[200:201], 0, s[28:29]
	s_mov_b32 m0, s49
	s_addc_u32 s23, s23, 0
	global_load_lds_dwordx4 v[198:199], off
	v_lshl_add_u64 v[198:199], s[22:23], 0, v[0:1]
	s_mov_b32 m0, s53
	s_nop 0
	global_load_lds_dwordx4 v[198:199], off
	v_lshl_add_u64 v[198:199], s[22:23], 0, v[208:209]
	s_mov_b32 m0, s54
	s_nop 0
	global_load_lds_dwordx4 v[198:199], off
	v_lshl_add_u64 v[198:199], v[214:215], 0, s[28:29]
	s_mov_b32 m0, s50
	s_nop 0
	global_load_lds_dwordx4 v[198:199], off
	v_lshl_add_u64 v[198:199], v[216:217], 0, s[28:29]
	s_mov_b32 m0, s51
	s_nop 0
	global_load_lds_dwordx4 v[198:199], off
	s_waitcnt vmcnt(8)
	s_waitcnt lgkmcnt(0)
	s_barrier
	s_setprio 1
	s_waitcnt lgkmcnt(0)
	v_mfma_f32_16x16x32_bf16 v[66:69], v[118:121], v[166:169], v[66:69]
	v_mfma_f32_16x16x32_bf16 v[62:65], v[130:133], v[166:169], v[62:65]
	v_mfma_f32_16x16x32_bf16 v[50:53], v[118:121], v[174:177], v[50:53]
	v_mfma_f32_16x16x32_bf16 v[46:49], v[130:133], v[174:177], v[46:49]
	v_mfma_f32_16x16x32_bf16 v[34:37], v[118:121], v[182:185], v[34:37]
	v_mfma_f32_16x16x32_bf16 v[30:33], v[130:133], v[182:185], v[30:33]
	v_mfma_f32_16x16x32_bf16 v[18:21], v[118:121], v[190:193], v[18:21]
	v_mfma_f32_16x16x32_bf16 v[14:17], v[130:133], v[190:193], v[14:17]
	v_mfma_f32_16x16x32_bf16 v[66:69], v[122:125], v[170:173], v[66:69]
	v_mfma_f32_16x16x32_bf16 v[62:65], v[138:141], v[170:173], v[62:65]
	v_mfma_f32_16x16x32_bf16 v[50:53], v[122:125], v[178:181], v[50:53]
	v_mfma_f32_16x16x32_bf16 v[46:49], v[138:141], v[178:181], v[46:49]
	v_mfma_f32_16x16x32_bf16 v[34:37], v[122:125], v[186:189], v[34:37]
	v_mfma_f32_16x16x32_bf16 v[30:33], v[138:141], v[186:189], v[30:33]
	v_mfma_f32_16x16x32_bf16 v[18:21], v[122:125], v[194:197], v[18:21]
	v_mfma_f32_16x16x32_bf16 v[14:17], v[138:141], v[194:197], v[14:17]
	s_setprio 0
	s_setprio 1
	v_mfma_f32_16x16x32_bf16 v[58:61], v[142:145], v[166:169], v[58:61]
	v_mfma_f32_16x16x32_bf16 v[54:57], v[154:157], v[166:169], v[54:57]
	v_mfma_f32_16x16x32_bf16 v[42:45], v[142:145], v[174:177], v[42:45]
	v_mfma_f32_16x16x32_bf16 v[38:41], v[154:157], v[174:177], v[38:41]
	v_mfma_f32_16x16x32_bf16 v[26:29], v[142:145], v[182:185], v[26:29]
	v_mfma_f32_16x16x32_bf16 v[22:25], v[154:157], v[182:185], v[22:25]
	v_mfma_f32_16x16x32_bf16 v[10:13], v[142:145], v[190:193], v[10:13]
	v_mfma_f32_16x16x32_bf16 v[6:9], v[154:157], v[190:193], v[6:9]
	v_mfma_f32_16x16x32_bf16 v[58:61], v[150:153], v[170:173], v[58:61]
	v_mfma_f32_16x16x32_bf16 v[54:57], v[162:165], v[170:173], v[54:57]
	v_mfma_f32_16x16x32_bf16 v[42:45], v[150:153], v[178:181], v[42:45]
	v_mfma_f32_16x16x32_bf16 v[38:41], v[162:165], v[178:181], v[38:41]
	v_mfma_f32_16x16x32_bf16 v[26:29], v[150:153], v[186:189], v[26:29]
	v_mfma_f32_16x16x32_bf16 v[22:25], v[162:165], v[186:189], v[22:25]
	s_setprio 2
	s_barrier
	v_mfma_f32_16x16x32_bf16 v[10:13], v[150:153], v[194:197], v[10:13]
	v_mfma_f32_16x16x32_bf16 v[6:9], v[162:165], v[194:197], v[6:9]
	s_setprio 0
	s_add_i32 s60, s60, 2
	s_add_u32 s58, s58, 0x100
	s_addc_u32 s59, s59, 0
	s_add_u32 s18, s18, 0x100
	s_addc_u32 s19, s19, 0
	s_cmp_gt_u32 s60, 13
	s_cbranch_scc0 .LBB0_1875
	s_branch .Lpeel_x__1875

.LBB0_1950:
	s_ashr_i32 s9, s8, 31
	s_lshl_b64 s[10:11], s[8:9], 20
	s_add_u32 s10, s4, s10
	s_addc_u32 s11, s5, s11
	s_and_b64 s[12:13], s[38:39], exec
	s_cselect_b32 s9, s11, s23
	s_cselect_b32 s15, s10, s22
	s_ashr_i32 s7, s6, 31
	s_lshl_b64 s[12:13], s[6:7], 20
	s_add_u32 s12, s21, s12
	s_addc_u32 s13, s30, s13
	s_and_b64 s[24:25], s[38:39], exec
	s_cselect_b32 s7, s13, s19
	s_cselect_b32 s17, s12, s18
	s_add_u32 s26, s18, 0x100
	s_addc_u32 s58, s19, 0
	s_add_u32 s18, s22, 0x80080
	v_mov_b32_e32 v6, 0
	s_addc_u32 s19, s23, 0
	s_mov_b32 s59, -2
	s_waitcnt lgkmcnt(0)
	v_add_u32_e32 v146, s31, v182
	v_add_u32_e32 v170, s40, v182
	ds_read_b128 v[134:137], v146
	ds_read_b128 v[138:141], v146 offset:1024
	ds_read_b128 v[142:145], v146 offset:2048
	ds_read_b128 v[146:149], v146 offset:3072
	ds_read_b128 v[150:153], v170
	ds_read_b128 v[154:157], v170 offset:1024
	ds_read_b128 v[158:161], v170 offset:2048
	ds_read_b128 v[170:173], v170 offset:3072
	s_add_u32 s22, s18, 0xfff80080
	s_addc_u32 s23, s19, -1
	s_cmp_eq_u32 s59, 28
	s_cselect_b32 s25, s9, s23
	s_cselect_b32 s24, s15, s22
	s_cselect_b32 s23, s7, s58
	s_cselect_b32 s22, s17, s26
	v_lshl_add_u64 v[214:215], s[18:19], 0, v[168:169]
	s_add_i32 m0, s43, 0xc000
	ds_read_b128 v[174:177], v184
	ds_read_b128 v[178:181], v184 offset:1024
	ds_read_b128 v[186:189], v184 offset:2048
	ds_read_b128 v[190:193], v184 offset:3072
	ds_read_b128 v[194:197], v184 offset:4096
	ds_read_b128 v[198:201], v184 offset:5120
	ds_read_b128 v[206:209], v184 offset:6144
	ds_read_b128 v[210:213], v184 offset:7168
	global_load_lds_dwordx4 v[214:215], off
	v_lshl_add_u64 v[214:215], s[18:19], 0, v[166:167]
	s_add_i32 m0, s43, 0xe000
	s_nop 0
	global_load_lds_dwordx4 v[214:215], off
	s_waitcnt vmcnt(8)
	s_waitcnt lgkmcnt(0)
	s_barrier
	s_setprio 1
	s_waitcnt lgkmcnt(0)
	v_mfma_f32_16x16x32_bf16 v[130:133], v[134:137], v[174:177], 0
	v_mfma_f32_16x16x32_bf16 v[126:129], v[142:145], v[174:177], 0
	v_mfma_f32_16x16x32_bf16 v[114:117], v[134:137], v[186:189], 0
	v_mfma_f32_16x16x32_bf16 v[110:113], v[142:145], v[186:189], 0
	v_mfma_f32_16x16x32_bf16 v[98:101], v[134:137], v[194:197], 0
	v_mfma_f32_16x16x32_bf16 v[94:97], v[142:145], v[194:197], 0
	v_mfma_f32_16x16x32_bf16 v[82:85], v[134:137], v[206:209], 0
	v_mfma_f32_16x16x32_bf16 v[78:81], v[142:145], v[206:209], 0
	v_mfma_f32_16x16x32_bf16 v[130:133], v[138:141], v[178:181], v[130:133]
	v_mfma_f32_16x16x32_bf16 v[126:129], v[146:149], v[178:181], v[126:129]
	v_mfma_f32_16x16x32_bf16 v[114:117], v[138:141], v[190:193], v[114:117]
	v_mfma_f32_16x16x32_bf16 v[110:113], v[146:149], v[190:193], v[110:113]
	v_mfma_f32_16x16x32_bf16 v[98:101], v[138:141], v[198:201], v[98:101]
	v_mfma_f32_16x16x32_bf16 v[94:97], v[146:149], v[198:201], v[94:97]
	v_mfma_f32_16x16x32_bf16 v[82:85], v[138:141], v[210:213], v[82:85]
	v_mfma_f32_16x16x32_bf16 v[78:81], v[146:149], v[210:213], v[78:81]
	s_setprio 0
	s_setprio 1
	v_mfma_f32_16x16x32_bf16 v[122:125], v[150:153], v[174:177], 0
	v_mfma_f32_16x16x32_bf16 v[118:121], v[158:161], v[174:177], 0
	v_mfma_f32_16x16x32_bf16 v[106:109], v[150:153], v[186:189], 0
	v_mfma_f32_16x16x32_bf16 v[102:105], v[158:161], v[186:189], 0
	v_mfma_f32_16x16x32_bf16 v[90:93], v[150:153], v[194:197], 0
	v_mfma_f32_16x16x32_bf16 v[86:89], v[158:161], v[194:197], 0
	v_mfma_f32_16x16x32_bf16 v[74:77], v[150:153], v[206:209], 0
	v_mfma_f32_16x16x32_bf16 v[70:73], v[158:161], v[206:209], 0
	v_mfma_f32_16x16x32_bf16 v[122:125], v[154:157], v[178:181], v[122:125]
	v_mfma_f32_16x16x32_bf16 v[118:121], v[170:173], v[178:181], v[118:121]
	v_mfma_f32_16x16x32_bf16 v[106:109], v[154:157], v[190:193], v[106:109]
	v_mfma_f32_16x16x32_bf16 v[102:105], v[170:173], v[190:193], v[102:105]
	v_mfma_f32_16x16x32_bf16 v[90:93], v[154:157], v[198:201], v[90:93]
	v_mfma_f32_16x16x32_bf16 v[86:89], v[170:173], v[198:201], v[86:89]
	s_setprio 2
	s_barrier
	v_mfma_f32_16x16x32_bf16 v[74:77], v[154:157], v[210:213], v[74:77]
	v_mfma_f32_16x16x32_bf16 v[70:73], v[170:173], v[210:213], v[70:73]
	s_setprio 0
	s_mov_b32 m0, s34
	v_lshl_add_u64 v[214:215], s[22:23], 0, v[0:1]
	s_add_u32 s60, s22, 0x80000
	ds_read_b128 v[174:177], v184 offset:16384
	ds_read_b128 v[178:181], v184 offset:17408
	ds_read_b128 v[186:189], v184 offset:18432
	ds_read_b128 v[190:193], v184 offset:19456
	ds_read_b128 v[194:197], v184 offset:20480
	ds_read_b128 v[198:201], v184 offset:21504
	ds_read_b128 v[206:209], v184 offset:22528
	ds_read_b128 v[210:213], v184 offset:23552
	global_load_lds_dwordx4 v[214:215], off
	v_lshl_add_u64 v[216:217], s[22:23], 0, v[164:165]
	s_mov_b32 m0, s35
	s_addc_u32 s61, s23, 0
	global_load_lds_dwordx4 v[216:217], off
	v_lshl_add_u64 v[218:219], s[60:61], 0, v[0:1]
	s_mov_b32 m0, s41
	v_lshl_add_u64 v[220:221], s[24:25], 0, v[162:163]
	global_load_lds_dwordx4 v[218:219], off
	v_lshl_add_u64 v[218:219], s[60:61], 0, v[164:165]
	s_mov_b32 m0, s42
	s_nop 0
	global_load_lds_dwordx4 v[218:219], off
	v_lshl_add_u64 v[218:219], s[24:25], 0, v[2:3]
	s_mov_b32 m0, s43
	s_nop 0
	global_load_lds_dwordx4 v[218:219], off
	s_mov_b32 m0, s44
	s_nop 0
	global_load_lds_dwordx4 v[220:221], off
	s_waitcnt vmcnt(8)
	s_waitcnt lgkmcnt(0)
	s_barrier
	s_setprio 1
	s_waitcnt lgkmcnt(0)
	v_mfma_f32_16x16x32_bf16 v[66:69], v[134:137], v[174:177], 0
	v_mfma_f32_16x16x32_bf16 v[62:65], v[142:145], v[174:177], 0
	v_mfma_f32_16x16x32_bf16 v[50:53], v[134:137], v[186:189], 0
	v_mfma_f32_16x16x32_bf16 v[46:49], v[142:145], v[186:189], 0
	v_mfma_f32_16x16x32_bf16 v[34:37], v[134:137], v[194:197], 0
	v_mfma_f32_16x16x32_bf16 v[30:33], v[142:145], v[194:197], 0
	v_mfma_f32_16x16x32_bf16 v[18:21], v[134:137], v[206:209], 0
	v_mfma_f32_16x16x32_bf16 v[14:17], v[142:145], v[206:209], 0
	v_mfma_f32_16x16x32_bf16 v[66:69], v[138:141], v[178:181], v[66:69]
	v_mfma_f32_16x16x32_bf16 v[62:65], v[146:149], v[178:181], v[62:65]
	v_mfma_f32_16x16x32_bf16 v[50:53], v[138:141], v[190:193], v[50:53]
	v_mfma_f32_16x16x32_bf16 v[46:49], v[146:149], v[190:193], v[46:49]
	v_mfma_f32_16x16x32_bf16 v[34:37], v[138:141], v[198:201], v[34:37]
	v_mfma_f32_16x16x32_bf16 v[30:33], v[146:149], v[198:201], v[30:33]
	v_mfma_f32_16x16x32_bf16 v[18:21], v[138:141], v[210:213], v[18:21]
	v_mfma_f32_16x16x32_bf16 v[14:17], v[146:149], v[210:213], v[14:17]
	s_setprio 0
	s_setprio 1
	v_mfma_f32_16x16x32_bf16 v[58:61], v[150:153], v[174:177], 0
	v_mfma_f32_16x16x32_bf16 v[54:57], v[158:161], v[174:177], 0
	v_mfma_f32_16x16x32_bf16 v[42:45], v[150:153], v[186:189], 0
	v_mfma_f32_16x16x32_bf16 v[38:41], v[158:161], v[186:189], 0
	v_mfma_f32_16x16x32_bf16 v[26:29], v[150:153], v[194:197], 0
	v_mfma_f32_16x16x32_bf16 v[22:25], v[158:161], v[194:197], 0
	v_mfma_f32_16x16x32_bf16 v[10:13], v[150:153], v[206:209], 0
	v_mfma_f32_16x16x32_bf16 v[6:9], v[158:161], v[206:209], 0
	v_mfma_f32_16x16x32_bf16 v[58:61], v[154:157], v[178:181], v[58:61]
	v_mfma_f32_16x16x32_bf16 v[54:57], v[170:173], v[178:181], v[54:57]
	v_mfma_f32_16x16x32_bf16 v[42:45], v[154:157], v[190:193], v[42:45]
	v_mfma_f32_16x16x32_bf16 v[38:41], v[170:173], v[190:193], v[38:41]
	v_mfma_f32_16x16x32_bf16 v[26:29], v[154:157], v[198:201], v[26:29]
	v_mfma_f32_16x16x32_bf16 v[22:25], v[170:173], v[198:201], v[22:25]
	s_setprio 2
	s_barrier
	v_mfma_f32_16x16x32_bf16 v[10:13], v[154:157], v[210:213], v[10:13]
	v_mfma_f32_16x16x32_bf16 v[6:9], v[170:173], v[210:213], v[6:9]
	s_setprio 0
	v_add_u32_e32 v146, s48, v182
	v_add_u32_e32 v170, s53, v182
	ds_read_b128 v[134:137], v146
	ds_read_b128 v[138:141], v146 offset:1024
	ds_read_b128 v[142:145], v146 offset:2048
	ds_read_b128 v[146:149], v146 offset:3072
	ds_read_b128 v[150:153], v170
	ds_read_b128 v[154:157], v170 offset:1024
	ds_read_b128 v[158:161], v170 offset:2048
	ds_read_b128 v[170:173], v170 offset:3072
	s_add_u32 s24, s24, 0x80000
	s_addc_u32 s25, s25, 0
	s_mov_b32 m0, s45
	v_lshl_add_u64 v[222:223], s[24:25], 0, v[2:3]
	ds_read_b128 v[174:177], v184 offset:32768
	ds_read_b128 v[178:181], v184 offset:33792
	ds_read_b128 v[186:189], v184 offset:34816
	ds_read_b128 v[190:193], v184 offset:35840
	ds_read_b128 v[194:197], v184 offset:36864
	ds_read_b128 v[198:201], v184 offset:37888
	ds_read_b128 v[206:209], v184 offset:38912
	ds_read_b128 v[210:213], v184 offset:39936
	global_load_lds_dwordx4 v[222:223], off
	v_lshl_add_u64 v[222:223], s[24:25], 0, v[162:163]
	s_mov_b32 m0, s46
	s_nop 0
	global_load_lds_dwordx4 v[222:223], off
	s_waitcnt vmcnt(8)
	s_waitcnt lgkmcnt(0)
	s_barrier
	s_setprio 1
	s_waitcnt lgkmcnt(0)
	v_mfma_f32_16x16x32_bf16 v[130:133], v[134:137], v[174:177], v[130:133]
	v_mfma_f32_16x16x32_bf16 v[126:129], v[142:145], v[174:177], v[126:129]
	v_mfma_f32_16x16x32_bf16 v[114:117], v[134:137], v[186:189], v[114:117]
	v_mfma_f32_16x16x32_bf16 v[110:113], v[142:145], v[186:189], v[110:113]
	v_mfma_f32_16x16x32_bf16 v[98:101], v[134:137], v[194:197], v[98:101]
	v_mfma_f32_16x16x32_bf16 v[94:97], v[142:145], v[194:197], v[94:97]
	v_mfma_f32_16x16x32_bf16 v[82:85], v[134:137], v[206:209], v[82:85]
	v_mfma_f32_16x16x32_bf16 v[78:81], v[142:145], v[206:209], v[78:81]
	v_mfma_f32_16x16x32_bf16 v[130:133], v[138:141], v[178:181], v[130:133]
	v_mfma_f32_16x16x32_bf16 v[126:129], v[146:149], v[178:181], v[126:129]
	v_mfma_f32_16x16x32_bf16 v[114:117], v[138:141], v[190:193], v[114:117]
	v_mfma_f32_16x16x32_bf16 v[110:113], v[146:149], v[190:193], v[110:113]
	v_mfma_f32_16x16x32_bf16 v[98:101], v[138:141], v[198:201], v[98:101]
	v_mfma_f32_16x16x32_bf16 v[94:97], v[146:149], v[198:201], v[94:97]
	v_mfma_f32_16x16x32_bf16 v[82:85], v[138:141], v[210:213], v[82:85]
	v_mfma_f32_16x16x32_bf16 v[78:81], v[146:149], v[210:213], v[78:81]
	s_setprio 0
	s_setprio 1
	v_mfma_f32_16x16x32_bf16 v[122:125], v[150:153], v[174:177], v[122:125]
	v_mfma_f32_16x16x32_bf16 v[118:121], v[158:161], v[174:177], v[118:121]
	v_mfma_f32_16x16x32_bf16 v[106:109], v[150:153], v[186:189], v[106:109]
	v_mfma_f32_16x16x32_bf16 v[102:105], v[158:161], v[186:189], v[102:105]
	v_mfma_f32_16x16x32_bf16 v[90:93], v[150:153], v[194:197], v[90:93]
	v_mfma_f32_16x16x32_bf16 v[86:89], v[158:161], v[194:197], v[86:89]
	v_mfma_f32_16x16x32_bf16 v[74:77], v[150:153], v[206:209], v[74:77]
	v_mfma_f32_16x16x32_bf16 v[70:73], v[158:161], v[206:209], v[70:73]
	v_mfma_f32_16x16x32_bf16 v[122:125], v[154:157], v[178:181], v[122:125]
	v_mfma_f32_16x16x32_bf16 v[118:121], v[170:173], v[178:181], v[118:121]
	v_mfma_f32_16x16x32_bf16 v[106:109], v[154:157], v[190:193], v[106:109]
	v_mfma_f32_16x16x32_bf16 v[102:105], v[170:173], v[190:193], v[102:105]
	v_mfma_f32_16x16x32_bf16 v[90:93], v[154:157], v[198:201], v[90:93]
	v_mfma_f32_16x16x32_bf16 v[86:89], v[170:173], v[198:201], v[86:89]
	s_setprio 2
	s_barrier
	v_mfma_f32_16x16x32_bf16 v[74:77], v[154:157], v[210:213], v[74:77]
	v_mfma_f32_16x16x32_bf16 v[70:73], v[170:173], v[210:213], v[70:73]
	s_setprio 0
	s_mov_b32 m0, s49
	v_lshl_add_u64 v[214:215], v[214:215], 0, s[28:29]
	s_add_u32 s22, s22, 0x80080
	ds_read_b128 v[174:177], v184 offset:49152
	ds_read_b128 v[178:181], v184 offset:50176
	ds_read_b128 v[186:189], v184 offset:51200
	ds_read_b128 v[190:193], v184 offset:52224
	ds_read_b128 v[194:197], v184 offset:53248
	ds_read_b128 v[198:201], v184 offset:54272
	ds_read_b128 v[206:209], v184 offset:55296
	ds_read_b128 v[210:213], v184 offset:56320
	global_load_lds_dwordx4 v[214:215], off
	v_lshl_add_u64 v[214:215], v[216:217], 0, s[28:29]
	s_mov_b32 m0, s50
	s_addc_u32 s23, s23, 0
	global_load_lds_dwordx4 v[214:215], off
	v_lshl_add_u64 v[214:215], s[22:23], 0, v[0:1]
	s_mov_b32 m0, s54
	s_nop 0
	global_load_lds_dwordx4 v[214:215], off
	v_lshl_add_u64 v[214:215], s[22:23], 0, v[164:165]
	s_mov_b32 m0, s55
	s_nop 0
	global_load_lds_dwordx4 v[214:215], off
	v_lshl_add_u64 v[214:215], v[218:219], 0, s[28:29]
	s_mov_b32 m0, s51
	s_nop 0
	global_load_lds_dwordx4 v[214:215], off
	v_lshl_add_u64 v[214:215], v[220:221], 0, s[28:29]
	s_mov_b32 m0, s52
	s_nop 0
	global_load_lds_dwordx4 v[214:215], off
	s_waitcnt vmcnt(8)
	s_waitcnt lgkmcnt(0)
	s_barrier
	s_setprio 1
	s_waitcnt lgkmcnt(0)
	v_mfma_f32_16x16x32_bf16 v[66:69], v[134:137], v[174:177], v[66:69]
	v_mfma_f32_16x16x32_bf16 v[62:65], v[142:145], v[174:177], v[62:65]
	v_mfma_f32_16x16x32_bf16 v[50:53], v[134:137], v[186:189], v[50:53]
	v_mfma_f32_16x16x32_bf16 v[46:49], v[142:145], v[186:189], v[46:49]
	v_mfma_f32_16x16x32_bf16 v[34:37], v[134:137], v[194:197], v[34:37]
	v_mfma_f32_16x16x32_bf16 v[30:33], v[142:145], v[194:197], v[30:33]
	v_mfma_f32_16x16x32_bf16 v[18:21], v[134:137], v[206:209], v[18:21]
	v_mfma_f32_16x16x32_bf16 v[14:17], v[142:145], v[206:209], v[14:17]
	v_mfma_f32_16x16x32_bf16 v[66:69], v[138:141], v[178:181], v[66:69]
	v_mfma_f32_16x16x32_bf16 v[62:65], v[146:149], v[178:181], v[62:65]
	v_mfma_f32_16x16x32_bf16 v[50:53], v[138:141], v[190:193], v[50:53]
	v_mfma_f32_16x16x32_bf16 v[46:49], v[146:149], v[190:193], v[46:49]
	v_mfma_f32_16x16x32_bf16 v[34:37], v[138:141], v[198:201], v[34:37]
	v_mfma_f32_16x16x32_bf16 v[30:33], v[146:149], v[198:201], v[30:33]
	v_mfma_f32_16x16x32_bf16 v[18:21], v[138:141], v[210:213], v[18:21]
	v_mfma_f32_16x16x32_bf16 v[14:17], v[146:149], v[210:213], v[14:17]
	s_setprio 0
	s_setprio 1
	v_mfma_f32_16x16x32_bf16 v[58:61], v[150:153], v[174:177], v[58:61]
	v_mfma_f32_16x16x32_bf16 v[54:57], v[158:161], v[174:177], v[54:57]
	v_mfma_f32_16x16x32_bf16 v[42:45], v[150:153], v[186:189], v[42:45]
	v_mfma_f32_16x16x32_bf16 v[38:41], v[158:161], v[186:189], v[38:41]
	v_mfma_f32_16x16x32_bf16 v[26:29], v[150:153], v[194:197], v[26:29]
	v_mfma_f32_16x16x32_bf16 v[22:25], v[158:161], v[194:197], v[22:25]
	v_mfma_f32_16x16x32_bf16 v[10:13], v[150:153], v[206:209], v[10:13]
	v_mfma_f32_16x16x32_bf16 v[6:9], v[158:161], v[206:209], v[6:9]
	v_mfma_f32_16x16x32_bf16 v[58:61], v[154:157], v[178:181], v[58:61]
	v_mfma_f32_16x16x32_bf16 v[54:57], v[170:173], v[178:181], v[54:57]
	v_mfma_f32_16x16x32_bf16 v[42:45], v[154:157], v[190:193], v[42:45]
	v_mfma_f32_16x16x32_bf16 v[38:41], v[170:173], v[190:193], v[38:41]
	v_mfma_f32_16x16x32_bf16 v[26:29], v[154:157], v[198:201], v[26:29]
	v_mfma_f32_16x16x32_bf16 v[22:25], v[170:173], v[198:201], v[22:25]
	s_setprio 2
	s_barrier
	v_mfma_f32_16x16x32_bf16 v[10:13], v[154:157], v[210:213], v[10:13]
	v_mfma_f32_16x16x32_bf16 v[6:9], v[170:173], v[210:213], v[6:9]
	s_setprio 0
	s_add_i32 s59, s59, 2
	s_add_u32 s26, s26, 0x100
	s_addc_u32 s58, s58, 0
	s_add_u32 s18, s18, 0x100
	s_addc_u32 s19, s19, 0
	s_cmp_gt_u32 s59, 29
	s_cbranch_scc0 .LBB0_1951
	s_branch .Lpeel_x__1951

.Lpeel_x__1951:
	s_and_b64 vcc, exec, s[2:3]
	s_cbranch_vccz .LBB0_1954
	s_barrier

.LBB0_2034:
	s_ashr_i32 s9, s8, 31
	s_lshl_b64 s[10:11], s[8:9], 20
	v_readlane_b32 s12, v254, 58
	v_readlane_b32 s13, v254, 59
	s_add_u32 s10, s12, s10
	s_addc_u32 s11, s13, s11
	s_and_b64 s[12:13], s[2:3], exec
	s_cselect_b32 s9, s11, s19
	s_cselect_b32 s50, s10, s18
	s_ashr_i32 s7, s6, 31
	s_lshl_b64 s[12:13], s[6:7], 20
	s_add_u32 s12, s21, s12
	s_addc_u32 s13, s24, s13
	s_and_b64 s[22:23], s[2:3], exec
	s_cselect_b32 s7, s13, s17
	s_cselect_b32 s51, s12, s16
	s_add_u32 s52, s16, 0x100
	s_addc_u32 s53, s17, 0
	s_add_u32 s16, s18, 0x80080
	v_mov_b32_e32 v6, 0
	s_addc_u32 s17, s19, 0
	s_mov_b32 s54, -2
	v_add_u32_e32 v142, s15, v144
	ds_read_b128 v[148:151], v142
	ds_read_b128 v[152:155], v142 offset:1024
	ds_read_b128 v[156:159], v142 offset:2048
	ds_read_b128 v[160:163], v142 offset:3072
	v_add_u32_e32 v142, s31, v144
	ds_read_b128 v[164:167], v142
	ds_read_b128 v[168:171], v142 offset:1024
	ds_read_b128 v[172:175], v142 offset:2048
	ds_read_b128 v[176:179], v142 offset:3072
	s_add_u32 s18, s16, 0xfff80080
	s_addc_u32 s19, s17, -1
	s_cmp_eq_u32 s54, 28
	s_cselect_b32 s23, s9, s19
	s_cselect_b32 s22, s50, s18
	s_cselect_b32 s19, s7, s53
	s_cselect_b32 s18, s51, s52
	v_lshl_add_u64 v[142:143], s[16:17], 0, v[140:141]
	s_add_i32 m0, s36, 0xc000
	ds_read_b128 v[180:183], v147
	ds_read_b128 v[184:187], v147 offset:1024
	ds_read_b128 v[188:191], v147 offset:2048
	ds_read_b128 v[192:195], v147 offset:3072
	ds_read_b128 v[196:199], v147 offset:4096
	ds_read_b128 v[206:209], v147 offset:5120
	ds_read_b128 v[210:213], v147 offset:6144
	ds_read_b128 v[214:217], v147 offset:7168
	global_load_lds_dwordx4 v[142:143], off
	v_lshl_add_u64 v[142:143], s[16:17], 0, v[138:139]
	s_add_i32 m0, s36, 0xe000
	s_nop 0
	global_load_lds_dwordx4 v[142:143], off
	s_waitcnt vmcnt(8)
	s_waitcnt lgkmcnt(0)
	s_barrier
	s_setprio 1
	s_waitcnt lgkmcnt(0)
	v_mfma_f32_16x16x32_bf16 v[130:133], v[148:151], v[180:183], 0
	v_mfma_f32_16x16x32_bf16 v[122:125], v[156:159], v[180:183], 0
	v_mfma_f32_16x16x32_bf16 v[114:117], v[148:151], v[188:191], 0
	v_mfma_f32_16x16x32_bf16 v[106:109], v[156:159], v[188:191], 0
	v_mfma_f32_16x16x32_bf16 v[98:101], v[148:151], v[196:199], 0
	v_mfma_f32_16x16x32_bf16 v[90:93], v[156:159], v[196:199], 0
	v_mfma_f32_16x16x32_bf16 v[82:85], v[148:151], v[210:213], 0
	v_mfma_f32_16x16x32_bf16 v[74:77], v[156:159], v[210:213], 0
	v_mfma_f32_16x16x32_bf16 v[130:133], v[152:155], v[184:187], v[130:133]
	v_mfma_f32_16x16x32_bf16 v[122:125], v[160:163], v[184:187], v[122:125]
	v_mfma_f32_16x16x32_bf16 v[114:117], v[152:155], v[192:195], v[114:117]
	v_mfma_f32_16x16x32_bf16 v[106:109], v[160:163], v[192:195], v[106:109]
	v_mfma_f32_16x16x32_bf16 v[98:101], v[152:155], v[206:209], v[98:101]
	v_mfma_f32_16x16x32_bf16 v[90:93], v[160:163], v[206:209], v[90:93]
	v_mfma_f32_16x16x32_bf16 v[82:85], v[152:155], v[214:217], v[82:85]
	v_mfma_f32_16x16x32_bf16 v[74:77], v[160:163], v[214:217], v[74:77]
	s_setprio 0
	s_setprio 1
	v_mfma_f32_16x16x32_bf16 v[126:129], v[164:167], v[180:183], 0
	v_mfma_f32_16x16x32_bf16 v[118:121], v[172:175], v[180:183], 0
	v_mfma_f32_16x16x32_bf16 v[110:113], v[164:167], v[188:191], 0
	v_mfma_f32_16x16x32_bf16 v[102:105], v[172:175], v[188:191], 0
	v_mfma_f32_16x16x32_bf16 v[94:97], v[164:167], v[196:199], 0
	v_mfma_f32_16x16x32_bf16 v[86:89], v[172:175], v[196:199], 0
	v_mfma_f32_16x16x32_bf16 v[78:81], v[164:167], v[210:213], 0
	v_mfma_f32_16x16x32_bf16 v[70:73], v[172:175], v[210:213], 0
	v_mfma_f32_16x16x32_bf16 v[126:129], v[168:171], v[184:187], v[126:129]
	v_mfma_f32_16x16x32_bf16 v[118:121], v[176:179], v[184:187], v[118:121]
	v_mfma_f32_16x16x32_bf16 v[110:113], v[168:171], v[192:195], v[110:113]
	v_mfma_f32_16x16x32_bf16 v[102:105], v[176:179], v[192:195], v[102:105]
	v_mfma_f32_16x16x32_bf16 v[94:97], v[168:171], v[206:209], v[94:97]
	v_mfma_f32_16x16x32_bf16 v[86:89], v[176:179], v[206:209], v[86:89]
	s_setprio 2
	s_barrier
	v_mfma_f32_16x16x32_bf16 v[78:81], v[168:171], v[214:217], v[78:81]
	v_mfma_f32_16x16x32_bf16 v[70:73], v[176:179], v[214:217], v[70:73]
	s_setprio 0
	s_mov_b32 m0, s26
	v_lshl_add_u64 v[142:143], s[18:19], 0, v[0:1]
	s_add_u32 s56, s18, 0x80000
	ds_read_b128 v[180:183], v147 offset:16384
	ds_read_b128 v[184:187], v147 offset:17408
	ds_read_b128 v[188:191], v147 offset:18432
	ds_read_b128 v[192:195], v147 offset:19456
	ds_read_b128 v[196:199], v147 offset:20480
	ds_read_b128 v[206:209], v147 offset:21504
	ds_read_b128 v[210:213], v147 offset:22528
	ds_read_b128 v[214:217], v147 offset:23552
	global_load_lds_dwordx4 v[142:143], off
	v_lshl_add_u64 v[200:201], s[18:19], 0, v[2:3]
	s_mov_b32 m0, s30
	s_addc_u32 s57, s19, 0
	global_load_lds_dwordx4 v[200:201], off
	v_lshl_add_u64 v[218:219], s[56:57], 0, v[0:1]
	s_mov_b32 m0, s34
	v_lshl_add_u64 v[220:221], s[22:23], 0, v[134:135]
	global_load_lds_dwordx4 v[218:219], off
	v_lshl_add_u64 v[218:219], s[56:57], 0, v[2:3]
	s_mov_b32 m0, s35
	s_nop 0
	global_load_lds_dwordx4 v[218:219], off
	v_lshl_add_u64 v[218:219], s[22:23], 0, v[136:137]
	s_mov_b32 m0, s36
	s_nop 0
	global_load_lds_dwordx4 v[218:219], off
	s_mov_b32 m0, s37
	s_nop 0
	global_load_lds_dwordx4 v[220:221], off
	s_waitcnt vmcnt(8)
	s_waitcnt lgkmcnt(0)
	s_barrier
	s_setprio 1
	s_waitcnt lgkmcnt(0)
	v_mfma_f32_16x16x32_bf16 v[66:69], v[148:151], v[180:183], 0
	v_mfma_f32_16x16x32_bf16 v[58:61], v[156:159], v[180:183], 0
	v_mfma_f32_16x16x32_bf16 v[50:53], v[148:151], v[188:191], 0
	v_mfma_f32_16x16x32_bf16 v[42:45], v[156:159], v[188:191], 0
	v_mfma_f32_16x16x32_bf16 v[34:37], v[148:151], v[196:199], 0
	v_mfma_f32_16x16x32_bf16 v[26:29], v[156:159], v[196:199], 0
	v_mfma_f32_16x16x32_bf16 v[18:21], v[148:151], v[210:213], 0
	v_mfma_f32_16x16x32_bf16 v[10:13], v[156:159], v[210:213], 0
	v_mfma_f32_16x16x32_bf16 v[66:69], v[152:155], v[184:187], v[66:69]
	v_mfma_f32_16x16x32_bf16 v[58:61], v[160:163], v[184:187], v[58:61]
	v_mfma_f32_16x16x32_bf16 v[50:53], v[152:155], v[192:195], v[50:53]
	v_mfma_f32_16x16x32_bf16 v[42:45], v[160:163], v[192:195], v[42:45]
	v_mfma_f32_16x16x32_bf16 v[34:37], v[152:155], v[206:209], v[34:37]
	v_mfma_f32_16x16x32_bf16 v[26:29], v[160:163], v[206:209], v[26:29]
	v_mfma_f32_16x16x32_bf16 v[18:21], v[152:155], v[214:217], v[18:21]
	v_mfma_f32_16x16x32_bf16 v[10:13], v[160:163], v[214:217], v[10:13]
	s_setprio 0
	s_setprio 1
	v_mfma_f32_16x16x32_bf16 v[62:65], v[164:167], v[180:183], 0
	v_mfma_f32_16x16x32_bf16 v[54:57], v[172:175], v[180:183], 0
	v_mfma_f32_16x16x32_bf16 v[46:49], v[164:167], v[188:191], 0
	v_mfma_f32_16x16x32_bf16 v[38:41], v[172:175], v[188:191], 0
	v_mfma_f32_16x16x32_bf16 v[30:33], v[164:167], v[196:199], 0
	v_mfma_f32_16x16x32_bf16 v[22:25], v[172:175], v[196:199], 0
	v_mfma_f32_16x16x32_bf16 v[14:17], v[164:167], v[210:213], 0
	v_mfma_f32_16x16x32_bf16 v[6:9], v[172:175], v[210:213], 0
	v_mfma_f32_16x16x32_bf16 v[62:65], v[168:171], v[184:187], v[62:65]
	v_mfma_f32_16x16x32_bf16 v[54:57], v[176:179], v[184:187], v[54:57]
	v_mfma_f32_16x16x32_bf16 v[46:49], v[168:171], v[192:195], v[46:49]
	v_mfma_f32_16x16x32_bf16 v[38:41], v[176:179], v[192:195], v[38:41]
	v_mfma_f32_16x16x32_bf16 v[30:33], v[168:171], v[206:209], v[30:33]
	v_mfma_f32_16x16x32_bf16 v[22:25], v[176:179], v[206:209], v[22:25]
	s_setprio 2
	s_barrier
	v_mfma_f32_16x16x32_bf16 v[14:17], v[168:171], v[214:217], v[14:17]
	v_mfma_f32_16x16x32_bf16 v[6:9], v[176:179], v[214:217], v[6:9]
	s_setprio 0
	v_add_u32_e32 v160, s40, v144
	v_add_u32_e32 v176, s45, v144
	ds_read_b128 v[148:151], v160
	ds_read_b128 v[152:155], v160 offset:1024
	ds_read_b128 v[156:159], v160 offset:2048
	ds_read_b128 v[160:163], v160 offset:3072
	ds_read_b128 v[164:167], v176
	ds_read_b128 v[168:171], v176 offset:1024
	ds_read_b128 v[172:175], v176 offset:2048
	ds_read_b128 v[176:179], v176 offset:3072
	s_add_u32 s22, s22, 0x80000
	s_addc_u32 s23, s23, 0
	s_mov_b32 m0, s38
	v_lshl_add_u64 v[222:223], s[22:23], 0, v[136:137]
	ds_read_b128 v[180:183], v147 offset:32768
	ds_read_b128 v[184:187], v147 offset:33792
	ds_read_b128 v[188:191], v147 offset:34816
	ds_read_b128 v[192:195], v147 offset:35840
	ds_read_b128 v[196:199], v147 offset:36864
	ds_read_b128 v[206:209], v147 offset:37888
	ds_read_b128 v[210:213], v147 offset:38912
	ds_read_b128 v[214:217], v147 offset:39936
	global_load_lds_dwordx4 v[222:223], off
	v_lshl_add_u64 v[222:223], s[22:23], 0, v[134:135]
	s_mov_b32 m0, s39
	s_nop 0
	global_load_lds_dwordx4 v[222:223], off
	s_waitcnt vmcnt(8)
	s_waitcnt lgkmcnt(0)
	s_barrier
	s_setprio 1
	s_waitcnt lgkmcnt(0)
	v_mfma_f32_16x16x32_bf16 v[130:133], v[148:151], v[180:183], v[130:133]
	v_mfma_f32_16x16x32_bf16 v[122:125], v[156:159], v[180:183], v[122:125]
	v_mfma_f32_16x16x32_bf16 v[114:117], v[148:151], v[188:191], v[114:117]
	v_mfma_f32_16x16x32_bf16 v[106:109], v[156:159], v[188:191], v[106:109]
	v_mfma_f32_16x16x32_bf16 v[98:101], v[148:151], v[196:199], v[98:101]
	v_mfma_f32_16x16x32_bf16 v[90:93], v[156:159], v[196:199], v[90:93]
	v_mfma_f32_16x16x32_bf16 v[82:85], v[148:151], v[210:213], v[82:85]
	v_mfma_f32_16x16x32_bf16 v[74:77], v[156:159], v[210:213], v[74:77]
	v_mfma_f32_16x16x32_bf16 v[130:133], v[152:155], v[184:187], v[130:133]
	v_mfma_f32_16x16x32_bf16 v[122:125], v[160:163], v[184:187], v[122:125]
	v_mfma_f32_16x16x32_bf16 v[114:117], v[152:155], v[192:195], v[114:117]
	v_mfma_f32_16x16x32_bf16 v[106:109], v[160:163], v[192:195], v[106:109]
	v_mfma_f32_16x16x32_bf16 v[98:101], v[152:155], v[206:209], v[98:101]
	v_mfma_f32_16x16x32_bf16 v[90:93], v[160:163], v[206:209], v[90:93]
	v_mfma_f32_16x16x32_bf16 v[82:85], v[152:155], v[214:217], v[82:85]
	v_mfma_f32_16x16x32_bf16 v[74:77], v[160:163], v[214:217], v[74:77]
	s_setprio 0
	s_setprio 1
	v_mfma_f32_16x16x32_bf16 v[126:129], v[164:167], v[180:183], v[126:129]
	v_mfma_f32_16x16x32_bf16 v[118:121], v[172:175], v[180:183], v[118:121]
	v_mfma_f32_16x16x32_bf16 v[110:113], v[164:167], v[188:191], v[110:113]
	v_mfma_f32_16x16x32_bf16 v[102:105], v[172:175], v[188:191], v[102:105]
	v_mfma_f32_16x16x32_bf16 v[94:97], v[164:167], v[196:199], v[94:97]
	v_mfma_f32_16x16x32_bf16 v[86:89], v[172:175], v[196:199], v[86:89]
	v_mfma_f32_16x16x32_bf16 v[78:81], v[164:167], v[210:213], v[78:81]
	v_mfma_f32_16x16x32_bf16 v[70:73], v[172:175], v[210:213], v[70:73]
	v_mfma_f32_16x16x32_bf16 v[126:129], v[168:171], v[184:187], v[126:129]
	v_mfma_f32_16x16x32_bf16 v[118:121], v[176:179], v[184:187], v[118:121]
	v_mfma_f32_16x16x32_bf16 v[110:113], v[168:171], v[192:195], v[110:113]
	v_mfma_f32_16x16x32_bf16 v[102:105], v[176:179], v[192:195], v[102:105]
	v_mfma_f32_16x16x32_bf16 v[94:97], v[168:171], v[206:209], v[94:97]
	v_mfma_f32_16x16x32_bf16 v[86:89], v[176:179], v[206:209], v[86:89]
	s_setprio 2
	s_barrier
	v_mfma_f32_16x16x32_bf16 v[78:81], v[168:171], v[214:217], v[78:81]
	v_mfma_f32_16x16x32_bf16 v[70:73], v[176:179], v[214:217], v[70:73]
	s_setprio 0
	s_mov_b32 m0, s41
	v_lshl_add_u64 v[142:143], v[142:143], 0, s[28:29]
	s_add_u32 s18, s18, 0x80080
	ds_read_b128 v[180:183], v147 offset:49152
	ds_read_b128 v[184:187], v147 offset:50176
	ds_read_b128 v[188:191], v147 offset:51200
	ds_read_b128 v[192:195], v147 offset:52224
	ds_read_b128 v[196:199], v147 offset:53248
	ds_read_b128 v[206:209], v147 offset:54272
	ds_read_b128 v[210:213], v147 offset:55296
	ds_read_b128 v[214:217], v147 offset:56320
	global_load_lds_dwordx4 v[142:143], off
	v_lshl_add_u64 v[142:143], v[200:201], 0, s[28:29]
	s_mov_b32 m0, s42
	s_addc_u32 s19, s19, 0
	global_load_lds_dwordx4 v[142:143], off
	v_lshl_add_u64 v[142:143], s[18:19], 0, v[0:1]
	s_mov_b32 m0, s46
	s_nop 0
	global_load_lds_dwordx4 v[142:143], off
	v_lshl_add_u64 v[142:143], s[18:19], 0, v[2:3]
	s_mov_b32 m0, s47
	s_nop 0
	global_load_lds_dwordx4 v[142:143], off
	v_lshl_add_u64 v[142:143], v[218:219], 0, s[28:29]
	s_mov_b32 m0, s43
	s_nop 0
	global_load_lds_dwordx4 v[142:143], off
	v_lshl_add_u64 v[142:143], v[220:221], 0, s[28:29]
	s_mov_b32 m0, s44
	s_nop 0
	global_load_lds_dwordx4 v[142:143], off
	s_waitcnt vmcnt(8)
	s_waitcnt lgkmcnt(0)
	s_barrier
	s_setprio 1
	s_waitcnt lgkmcnt(0)
	v_mfma_f32_16x16x32_bf16 v[66:69], v[148:151], v[180:183], v[66:69]
	v_mfma_f32_16x16x32_bf16 v[58:61], v[156:159], v[180:183], v[58:61]
	v_mfma_f32_16x16x32_bf16 v[50:53], v[148:151], v[188:191], v[50:53]
	v_mfma_f32_16x16x32_bf16 v[42:45], v[156:159], v[188:191], v[42:45]
	v_mfma_f32_16x16x32_bf16 v[34:37], v[148:151], v[196:199], v[34:37]
	v_mfma_f32_16x16x32_bf16 v[26:29], v[156:159], v[196:199], v[26:29]
	v_mfma_f32_16x16x32_bf16 v[18:21], v[148:151], v[210:213], v[18:21]
	v_mfma_f32_16x16x32_bf16 v[10:13], v[156:159], v[210:213], v[10:13]
	v_mfma_f32_16x16x32_bf16 v[66:69], v[152:155], v[184:187], v[66:69]
	v_mfma_f32_16x16x32_bf16 v[58:61], v[160:163], v[184:187], v[58:61]
	v_mfma_f32_16x16x32_bf16 v[50:53], v[152:155], v[192:195], v[50:53]
	v_mfma_f32_16x16x32_bf16 v[42:45], v[160:163], v[192:195], v[42:45]
	v_mfma_f32_16x16x32_bf16 v[34:37], v[152:155], v[206:209], v[34:37]
	v_mfma_f32_16x16x32_bf16 v[26:29], v[160:163], v[206:209], v[26:29]
	v_mfma_f32_16x16x32_bf16 v[18:21], v[152:155], v[214:217], v[18:21]
	v_mfma_f32_16x16x32_bf16 v[10:13], v[160:163], v[214:217], v[10:13]
	s_setprio 0
	s_setprio 1
	v_mfma_f32_16x16x32_bf16 v[62:65], v[164:167], v[180:183], v[62:65]
	v_mfma_f32_16x16x32_bf16 v[54:57], v[172:175], v[180:183], v[54:57]
	v_mfma_f32_16x16x32_bf16 v[46:49], v[164:167], v[188:191], v[46:49]
	v_mfma_f32_16x16x32_bf16 v[38:41], v[172:175], v[188:191], v[38:41]
	v_mfma_f32_16x16x32_bf16 v[30:33], v[164:167], v[196:199], v[30:33]
	v_mfma_f32_16x16x32_bf16 v[22:25], v[172:175], v[196:199], v[22:25]
	v_mfma_f32_16x16x32_bf16 v[14:17], v[164:167], v[210:213], v[14:17]
	v_mfma_f32_16x16x32_bf16 v[6:9], v[172:175], v[210:213], v[6:9]
	v_mfma_f32_16x16x32_bf16 v[62:65], v[168:171], v[184:187], v[62:65]
	v_mfma_f32_16x16x32_bf16 v[54:57], v[176:179], v[184:187], v[54:57]
	v_mfma_f32_16x16x32_bf16 v[46:49], v[168:171], v[192:195], v[46:49]
	v_mfma_f32_16x16x32_bf16 v[38:41], v[176:179], v[192:195], v[38:41]
	v_mfma_f32_16x16x32_bf16 v[30:33], v[168:171], v[206:209], v[30:33]
	v_mfma_f32_16x16x32_bf16 v[22:25], v[176:179], v[206:209], v[22:25]
	s_setprio 2
	s_barrier
	v_mfma_f32_16x16x32_bf16 v[14:17], v[168:171], v[214:217], v[14:17]
	v_mfma_f32_16x16x32_bf16 v[6:9], v[176:179], v[214:217], v[6:9]
	s_setprio 0
	s_add_i32 s54, s54, 2
	s_add_u32 s52, s52, 0x100
	s_addc_u32 s53, s53, 0
	s_add_u32 s16, s16, 0x100
	s_addc_u32 s17, s17, 0
	s_cmp_gt_u32 s54, 29
	s_cbranch_scc0 .LBB0_2035
	s_branch .Lpeel_x__2035

.LBB0_2113:
	s_add_u32 s53, s10, 0x100
	v_mov_b32_e32 v6, 0
	s_addc_u32 s54, s11, 0
	s_mov_b32 s55, -2
	s_waitcnt lgkmcnt(0)
	v_add_u32_e32 v146, s19, v182
	v_add_u32_e32 v170, s22, v182
	ds_read_b128 v[134:137], v146
	ds_read_b128 v[138:141], v146 offset:1024
	ds_read_b128 v[142:145], v146 offset:2048
	ds_read_b128 v[146:149], v146 offset:3072
	ds_read_b128 v[150:153], v170
	ds_read_b128 v[154:157], v170 offset:1024
	ds_read_b128 v[158:161], v170 offset:2048
	ds_read_b128 v[170:173], v170 offset:3072
	s_add_u32 s10, s8, 0x100
	s_addc_u32 s11, s9, 0
	s_cmpk_eq_i32 s55, 0x52
	s_cselect_b32 s15, s3, s11
	s_cselect_b32 s14, s2, s10
	s_cselect_b32 s13, s7, s54
	s_cselect_b32 s12, s6, s53
	v_lshl_add_u64 v[214:215], s[8:9], 0, v[168:169]
	s_add_i32 m0, s25, 0xc000
	ds_read_b128 v[174:177], v184
	ds_read_b128 v[178:181], v184 offset:1024
	ds_read_b128 v[186:189], v184 offset:2048
	ds_read_b128 v[190:193], v184 offset:3072
	ds_read_b128 v[194:197], v184 offset:4096
	ds_read_b128 v[198:201], v184 offset:5120
	ds_read_b128 v[206:209], v184 offset:6144
	ds_read_b128 v[210:213], v184 offset:7168
	global_load_lds_dwordx4 v[214:215], off
	v_lshl_add_u64 v[214:215], s[8:9], 0, v[166:167]
	s_add_i32 m0, s25, 0xe000
	s_nop 0
	global_load_lds_dwordx4 v[214:215], off
	s_waitcnt vmcnt(8)
	s_waitcnt lgkmcnt(0)
	s_barrier
	s_setprio 1
	s_waitcnt lgkmcnt(0)
	v_mfma_f32_16x16x32_bf16 v[130:133], v[134:137], v[174:177], 0
	v_mfma_f32_16x16x32_bf16 v[126:129], v[142:145], v[174:177], 0
	v_mfma_f32_16x16x32_bf16 v[114:117], v[134:137], v[186:189], 0
	v_mfma_f32_16x16x32_bf16 v[110:113], v[142:145], v[186:189], 0
	v_mfma_f32_16x16x32_bf16 v[98:101], v[134:137], v[194:197], 0
	v_mfma_f32_16x16x32_bf16 v[94:97], v[142:145], v[194:197], 0
	v_mfma_f32_16x16x32_bf16 v[82:85], v[134:137], v[206:209], 0
	v_mfma_f32_16x16x32_bf16 v[78:81], v[142:145], v[206:209], 0
	v_mfma_f32_16x16x32_bf16 v[130:133], v[138:141], v[178:181], v[130:133]
	v_mfma_f32_16x16x32_bf16 v[126:129], v[146:149], v[178:181], v[126:129]
	v_mfma_f32_16x16x32_bf16 v[114:117], v[138:141], v[190:193], v[114:117]
	v_mfma_f32_16x16x32_bf16 v[110:113], v[146:149], v[190:193], v[110:113]
	v_mfma_f32_16x16x32_bf16 v[98:101], v[138:141], v[198:201], v[98:101]
	v_mfma_f32_16x16x32_bf16 v[94:97], v[146:149], v[198:201], v[94:97]
	v_mfma_f32_16x16x32_bf16 v[82:85], v[138:141], v[210:213], v[82:85]
	v_mfma_f32_16x16x32_bf16 v[78:81], v[146:149], v[210:213], v[78:81]
	s_setprio 0
	s_setprio 1
	v_mfma_f32_16x16x32_bf16 v[122:125], v[150:153], v[174:177], 0
	v_mfma_f32_16x16x32_bf16 v[118:121], v[158:161], v[174:177], 0
	v_mfma_f32_16x16x32_bf16 v[106:109], v[150:153], v[186:189], 0
	v_mfma_f32_16x16x32_bf16 v[102:105], v[158:161], v[186:189], 0
	v_mfma_f32_16x16x32_bf16 v[90:93], v[150:153], v[194:197], 0
	v_mfma_f32_16x16x32_bf16 v[86:89], v[158:161], v[194:197], 0
	v_mfma_f32_16x16x32_bf16 v[74:77], v[150:153], v[206:209], 0
	v_mfma_f32_16x16x32_bf16 v[70:73], v[158:161], v[206:209], 0
	v_mfma_f32_16x16x32_bf16 v[122:125], v[154:157], v[178:181], v[122:125]
	v_mfma_f32_16x16x32_bf16 v[118:121], v[170:173], v[178:181], v[118:121]
	v_mfma_f32_16x16x32_bf16 v[106:109], v[154:157], v[190:193], v[106:109]
	v_mfma_f32_16x16x32_bf16 v[102:105], v[170:173], v[190:193], v[102:105]
	v_mfma_f32_16x16x32_bf16 v[90:93], v[154:157], v[198:201], v[90:93]
	v_mfma_f32_16x16x32_bf16 v[86:89], v[170:173], v[198:201], v[86:89]
	s_setprio 2
	s_barrier
	v_mfma_f32_16x16x32_bf16 v[74:77], v[154:157], v[210:213], v[74:77]
	v_mfma_f32_16x16x32_bf16 v[70:73], v[170:173], v[210:213], v[70:73]
	s_setprio 0
	s_mov_b32 m0, s20
	v_lshl_add_u64 v[214:215], s[12:13], 0, v[0:1]
	s_add_u32 s8, s12, 0x158000
	ds_read_b128 v[174:177], v184 offset:16384
	ds_read_b128 v[178:181], v184 offset:17408
	ds_read_b128 v[186:189], v184 offset:18432
	ds_read_b128 v[190:193], v184 offset:19456
	ds_read_b128 v[194:197], v184 offset:20480
	ds_read_b128 v[198:201], v184 offset:21504
	ds_read_b128 v[206:209], v184 offset:22528
	ds_read_b128 v[210:213], v184 offset:23552
	global_load_lds_dwordx4 v[214:215], off
	v_lshl_add_u64 v[216:217], s[12:13], 0, v[164:165]
	s_mov_b32 m0, s21
	s_addc_u32 s9, s13, 0
	global_load_lds_dwordx4 v[216:217], off
	v_lshl_add_u64 v[218:219], s[8:9], 0, v[0:1]
	s_mov_b32 m0, s23
	v_lshl_add_u64 v[220:221], s[14:15], 0, v[162:163]
	global_load_lds_dwordx4 v[218:219], off
	v_lshl_add_u64 v[218:219], s[8:9], 0, v[164:165]
	s_mov_b32 m0, s24
	s_nop 0
	global_load_lds_dwordx4 v[218:219], off
	v_lshl_add_u64 v[218:219], s[14:15], 0, v[2:3]
	s_mov_b32 m0, s25
	s_nop 0
	global_load_lds_dwordx4 v[218:219], off
	s_mov_b32 m0, s30
	s_nop 0
	global_load_lds_dwordx4 v[220:221], off
	s_waitcnt vmcnt(8)
	s_waitcnt lgkmcnt(0)
	s_barrier
	s_setprio 1
	s_waitcnt lgkmcnt(0)
	v_mfma_f32_16x16x32_bf16 v[66:69], v[134:137], v[174:177], 0
	v_mfma_f32_16x16x32_bf16 v[62:65], v[142:145], v[174:177], 0
	v_mfma_f32_16x16x32_bf16 v[50:53], v[134:137], v[186:189], 0
	v_mfma_f32_16x16x32_bf16 v[46:49], v[142:145], v[186:189], 0
	v_mfma_f32_16x16x32_bf16 v[34:37], v[134:137], v[194:197], 0
	v_mfma_f32_16x16x32_bf16 v[30:33], v[142:145], v[194:197], 0
	v_mfma_f32_16x16x32_bf16 v[18:21], v[134:137], v[206:209], 0
	v_mfma_f32_16x16x32_bf16 v[14:17], v[142:145], v[206:209], 0
	v_mfma_f32_16x16x32_bf16 v[66:69], v[138:141], v[178:181], v[66:69]
	v_mfma_f32_16x16x32_bf16 v[62:65], v[146:149], v[178:181], v[62:65]
	v_mfma_f32_16x16x32_bf16 v[50:53], v[138:141], v[190:193], v[50:53]
	v_mfma_f32_16x16x32_bf16 v[46:49], v[146:149], v[190:193], v[46:49]
	v_mfma_f32_16x16x32_bf16 v[34:37], v[138:141], v[198:201], v[34:37]
	v_mfma_f32_16x16x32_bf16 v[30:33], v[146:149], v[198:201], v[30:33]
	v_mfma_f32_16x16x32_bf16 v[18:21], v[138:141], v[210:213], v[18:21]
	v_mfma_f32_16x16x32_bf16 v[14:17], v[146:149], v[210:213], v[14:17]
	s_setprio 0
	s_setprio 1
	v_mfma_f32_16x16x32_bf16 v[58:61], v[150:153], v[174:177], 0
	v_mfma_f32_16x16x32_bf16 v[54:57], v[158:161], v[174:177], 0
	v_mfma_f32_16x16x32_bf16 v[42:45], v[150:153], v[186:189], 0
	v_mfma_f32_16x16x32_bf16 v[38:41], v[158:161], v[186:189], 0
	v_mfma_f32_16x16x32_bf16 v[26:29], v[150:153], v[194:197], 0
	v_mfma_f32_16x16x32_bf16 v[22:25], v[158:161], v[194:197], 0
	v_mfma_f32_16x16x32_bf16 v[10:13], v[150:153], v[206:209], 0
	v_mfma_f32_16x16x32_bf16 v[6:9], v[158:161], v[206:209], 0
	v_mfma_f32_16x16x32_bf16 v[58:61], v[154:157], v[178:181], v[58:61]
	v_mfma_f32_16x16x32_bf16 v[54:57], v[170:173], v[178:181], v[54:57]
	v_mfma_f32_16x16x32_bf16 v[42:45], v[154:157], v[190:193], v[42:45]
	v_mfma_f32_16x16x32_bf16 v[38:41], v[170:173], v[190:193], v[38:41]
	v_mfma_f32_16x16x32_bf16 v[26:29], v[154:157], v[198:201], v[26:29]
	v_mfma_f32_16x16x32_bf16 v[22:25], v[170:173], v[198:201], v[22:25]
	s_setprio 2
	s_barrier
	v_mfma_f32_16x16x32_bf16 v[10:13], v[154:157], v[210:213], v[10:13]
	v_mfma_f32_16x16x32_bf16 v[6:9], v[170:173], v[210:213], v[6:9]
	s_setprio 0
	v_add_u32_e32 v146, s40, v182
	v_add_u32_e32 v170, s45, v182
	ds_read_b128 v[134:137], v146
	ds_read_b128 v[138:141], v146 offset:1024
	ds_read_b128 v[142:145], v146 offset:2048
	ds_read_b128 v[146:149], v146 offset:3072
	ds_read_b128 v[150:153], v170
	ds_read_b128 v[154:157], v170 offset:1024
	ds_read_b128 v[158:161], v170 offset:2048
	ds_read_b128 v[170:173], v170 offset:3072
	s_add_u32 s8, s14, 0x280000
	s_addc_u32 s9, s15, 0
	s_mov_b32 m0, s31
	v_lshl_add_u64 v[222:223], s[8:9], 0, v[2:3]
	ds_read_b128 v[174:177], v184 offset:32768
	ds_read_b128 v[178:181], v184 offset:33792
	ds_read_b128 v[186:189], v184 offset:34816
	ds_read_b128 v[190:193], v184 offset:35840
	ds_read_b128 v[194:197], v184 offset:36864
	ds_read_b128 v[198:201], v184 offset:37888
	ds_read_b128 v[206:209], v184 offset:38912
	ds_read_b128 v[210:213], v184 offset:39936
	global_load_lds_dwordx4 v[222:223], off
	v_lshl_add_u64 v[222:223], s[8:9], 0, v[162:163]
	s_mov_b32 m0, s34
	s_nop 0
	global_load_lds_dwordx4 v[222:223], off
	s_waitcnt vmcnt(8)
	s_waitcnt lgkmcnt(0)
	s_barrier
	s_setprio 1
	s_waitcnt lgkmcnt(0)
	v_mfma_f32_16x16x32_bf16 v[130:133], v[134:137], v[174:177], v[130:133]
	v_mfma_f32_16x16x32_bf16 v[126:129], v[142:145], v[174:177], v[126:129]
	v_mfma_f32_16x16x32_bf16 v[114:117], v[134:137], v[186:189], v[114:117]
	v_mfma_f32_16x16x32_bf16 v[110:113], v[142:145], v[186:189], v[110:113]
	v_mfma_f32_16x16x32_bf16 v[98:101], v[134:137], v[194:197], v[98:101]
	v_mfma_f32_16x16x32_bf16 v[94:97], v[142:145], v[194:197], v[94:97]
	v_mfma_f32_16x16x32_bf16 v[82:85], v[134:137], v[206:209], v[82:85]
	v_mfma_f32_16x16x32_bf16 v[78:81], v[142:145], v[206:209], v[78:81]
	v_mfma_f32_16x16x32_bf16 v[130:133], v[138:141], v[178:181], v[130:133]
	v_mfma_f32_16x16x32_bf16 v[126:129], v[146:149], v[178:181], v[126:129]
	v_mfma_f32_16x16x32_bf16 v[114:117], v[138:141], v[190:193], v[114:117]
	v_mfma_f32_16x16x32_bf16 v[110:113], v[146:149], v[190:193], v[110:113]
	v_mfma_f32_16x16x32_bf16 v[98:101], v[138:141], v[198:201], v[98:101]
	v_mfma_f32_16x16x32_bf16 v[94:97], v[146:149], v[198:201], v[94:97]
	v_mfma_f32_16x16x32_bf16 v[82:85], v[138:141], v[210:213], v[82:85]
	v_mfma_f32_16x16x32_bf16 v[78:81], v[146:149], v[210:213], v[78:81]
	s_setprio 0
	s_setprio 1
	v_mfma_f32_16x16x32_bf16 v[122:125], v[150:153], v[174:177], v[122:125]
	v_mfma_f32_16x16x32_bf16 v[118:121], v[158:161], v[174:177], v[118:121]
	v_mfma_f32_16x16x32_bf16 v[106:109], v[150:153], v[186:189], v[106:109]
	v_mfma_f32_16x16x32_bf16 v[102:105], v[158:161], v[186:189], v[102:105]
	v_mfma_f32_16x16x32_bf16 v[90:93], v[150:153], v[194:197], v[90:93]
	v_mfma_f32_16x16x32_bf16 v[86:89], v[158:161], v[194:197], v[86:89]
	v_mfma_f32_16x16x32_bf16 v[74:77], v[150:153], v[206:209], v[74:77]
	v_mfma_f32_16x16x32_bf16 v[70:73], v[158:161], v[206:209], v[70:73]
	v_mfma_f32_16x16x32_bf16 v[122:125], v[154:157], v[178:181], v[122:125]
	v_mfma_f32_16x16x32_bf16 v[118:121], v[170:173], v[178:181], v[118:121]
	v_mfma_f32_16x16x32_bf16 v[106:109], v[154:157], v[190:193], v[106:109]
	v_mfma_f32_16x16x32_bf16 v[102:105], v[170:173], v[190:193], v[102:105]
	v_mfma_f32_16x16x32_bf16 v[90:93], v[154:157], v[198:201], v[90:93]
	v_mfma_f32_16x16x32_bf16 v[86:89], v[170:173], v[198:201], v[86:89]
	s_setprio 2
	s_barrier
	v_mfma_f32_16x16x32_bf16 v[74:77], v[154:157], v[210:213], v[74:77]
	v_mfma_f32_16x16x32_bf16 v[70:73], v[170:173], v[210:213], v[70:73]
	s_setprio 0
	s_mov_b32 m0, s41
	v_lshl_add_u64 v[214:215], v[214:215], 0, s[28:29]
	s_add_u32 s8, s12, 0x158080
	ds_read_b128 v[174:177], v184 offset:49152
	ds_read_b128 v[178:181], v184 offset:50176
	ds_read_b128 v[186:189], v184 offset:51200
	ds_read_b128 v[190:193], v184 offset:52224
	ds_read_b128 v[194:197], v184 offset:53248
	ds_read_b128 v[198:201], v184 offset:54272
	ds_read_b128 v[206:209], v184 offset:55296
	ds_read_b128 v[210:213], v184 offset:56320
	global_load_lds_dwordx4 v[214:215], off
	v_lshl_add_u64 v[214:215], v[216:217], 0, s[28:29]
	s_mov_b32 m0, s42
	s_addc_u32 s9, s13, 0
	global_load_lds_dwordx4 v[214:215], off
	v_lshl_add_u64 v[214:215], s[8:9], 0, v[0:1]
	s_mov_b32 m0, s46
	s_nop 0
	global_load_lds_dwordx4 v[214:215], off
	v_lshl_add_u64 v[214:215], s[8:9], 0, v[164:165]
	s_mov_b32 m0, s47
	s_nop 0
	global_load_lds_dwordx4 v[214:215], off
	v_lshl_add_u64 v[214:215], v[218:219], 0, s[28:29]
	s_mov_b32 m0, s43
	s_nop 0
	global_load_lds_dwordx4 v[214:215], off
	v_lshl_add_u64 v[214:215], v[220:221], 0, s[28:29]
	s_mov_b32 m0, s44
	s_nop 0
	global_load_lds_dwordx4 v[214:215], off
	s_waitcnt vmcnt(8)
	s_waitcnt lgkmcnt(0)
	s_barrier
	s_setprio 1
	s_waitcnt lgkmcnt(0)
	v_mfma_f32_16x16x32_bf16 v[66:69], v[134:137], v[174:177], v[66:69]
	v_mfma_f32_16x16x32_bf16 v[62:65], v[142:145], v[174:177], v[62:65]
	v_mfma_f32_16x16x32_bf16 v[50:53], v[134:137], v[186:189], v[50:53]
	v_mfma_f32_16x16x32_bf16 v[46:49], v[142:145], v[186:189], v[46:49]
	v_mfma_f32_16x16x32_bf16 v[34:37], v[134:137], v[194:197], v[34:37]
	v_mfma_f32_16x16x32_bf16 v[30:33], v[142:145], v[194:197], v[30:33]
	v_mfma_f32_16x16x32_bf16 v[18:21], v[134:137], v[206:209], v[18:21]
	v_mfma_f32_16x16x32_bf16 v[14:17], v[142:145], v[206:209], v[14:17]
	v_mfma_f32_16x16x32_bf16 v[66:69], v[138:141], v[178:181], v[66:69]
	v_mfma_f32_16x16x32_bf16 v[62:65], v[146:149], v[178:181], v[62:65]
	v_mfma_f32_16x16x32_bf16 v[50:53], v[138:141], v[190:193], v[50:53]
	v_mfma_f32_16x16x32_bf16 v[46:49], v[146:149], v[190:193], v[46:49]
	v_mfma_f32_16x16x32_bf16 v[34:37], v[138:141], v[198:201], v[34:37]
	v_mfma_f32_16x16x32_bf16 v[30:33], v[146:149], v[198:201], v[30:33]
	v_mfma_f32_16x16x32_bf16 v[18:21], v[138:141], v[210:213], v[18:21]
	v_mfma_f32_16x16x32_bf16 v[14:17], v[146:149], v[210:213], v[14:17]
	s_setprio 0
	s_setprio 1
	v_mfma_f32_16x16x32_bf16 v[58:61], v[150:153], v[174:177], v[58:61]
	v_mfma_f32_16x16x32_bf16 v[54:57], v[158:161], v[174:177], v[54:57]
	v_mfma_f32_16x16x32_bf16 v[42:45], v[150:153], v[186:189], v[42:45]
	v_mfma_f32_16x16x32_bf16 v[38:41], v[158:161], v[186:189], v[38:41]
	v_mfma_f32_16x16x32_bf16 v[26:29], v[150:153], v[194:197], v[26:29]
	v_mfma_f32_16x16x32_bf16 v[22:25], v[158:161], v[194:197], v[22:25]
	v_mfma_f32_16x16x32_bf16 v[10:13], v[150:153], v[206:209], v[10:13]
	v_mfma_f32_16x16x32_bf16 v[6:9], v[158:161], v[206:209], v[6:9]
	v_mfma_f32_16x16x32_bf16 v[58:61], v[154:157], v[178:181], v[58:61]
	v_mfma_f32_16x16x32_bf16 v[54:57], v[170:173], v[178:181], v[54:57]
	v_mfma_f32_16x16x32_bf16 v[42:45], v[154:157], v[190:193], v[42:45]
	v_mfma_f32_16x16x32_bf16 v[38:41], v[170:173], v[190:193], v[38:41]
	v_mfma_f32_16x16x32_bf16 v[26:29], v[154:157], v[198:201], v[26:29]
	v_mfma_f32_16x16x32_bf16 v[22:25], v[170:173], v[198:201], v[22:25]
	s_setprio 2
	s_barrier
	v_mfma_f32_16x16x32_bf16 v[10:13], v[154:157], v[210:213], v[10:13]
	v_mfma_f32_16x16x32_bf16 v[6:9], v[170:173], v[210:213], v[6:9]
	s_setprio 0
	s_add_i32 s55, s55, 2
	s_add_u32 s53, s53, 0x100
	s_addc_u32 s54, s54, 0
	s_cmpk_gt_u32 s55, 0x53
	s_mov_b64 s[8:9], s[10:11]
	s_cbranch_scc0 .LBB0_2114
	s_branch .Lpeel_x__2114

.LBB0_2159:
	s_add_u32 s50, s10, 0x100
	v_mov_b32_e32 v6, 0
	s_addc_u32 s51, s11, 0
	s_mov_b32 s52, -2
	v_add_u32_e32 v146, s20, v172
	v_add_u32_e32 v170, s23, v172
	ds_read_b128 v[134:137], v146
	ds_read_b128 v[138:141], v146 offset:1024
	ds_read_b128 v[142:145], v146 offset:2048
	ds_read_b128 v[146:149], v146 offset:3072
	ds_read_b128 v[150:153], v170
	ds_read_b128 v[162:165], v170 offset:1024
	ds_read_b128 v[166:169], v170 offset:2048
	ds_read_b128 v[176:179], v170 offset:3072
	s_add_u32 s10, s8, 0x100
	s_addc_u32 s11, s9, 0
	s_cmpk_eq_i32 s52, 0x52
	s_cselect_b32 s15, s3, s11
	s_cselect_b32 s14, s2, s10
	s_cselect_b32 s13, s7, s51
	s_cselect_b32 s12, s6, s50
	v_lshl_add_u64 v[170:171], s[8:9], 0, v[160:161]
	s_add_i32 m0, s26, 0xc000
	ds_read_b128 v[180:183], v174
	ds_read_b128 v[184:187], v174 offset:1024
	ds_read_b128 v[188:191], v174 offset:2048
	ds_read_b128 v[192:195], v174 offset:3072
	ds_read_b128 v[196:199], v174 offset:4096
	ds_read_b128 v[206:209], v174 offset:5120
	ds_read_b128 v[210:213], v174 offset:6144
	ds_read_b128 v[214:217], v174 offset:7168
	global_load_lds_dwordx4 v[170:171], off
	v_lshl_add_u64 v[170:171], s[8:9], 0, v[158:159]
	s_add_i32 m0, s26, 0xe000
	s_nop 0
	global_load_lds_dwordx4 v[170:171], off
	s_waitcnt vmcnt(8)
	s_waitcnt lgkmcnt(0)
	s_barrier
	s_setprio 1
	s_waitcnt lgkmcnt(0)
	v_mfma_f32_16x16x32_bf16 v[130:133], v[134:137], v[180:183], 0
	v_mfma_f32_16x16x32_bf16 v[126:129], v[142:145], v[180:183], 0
	v_mfma_f32_16x16x32_bf16 v[122:125], v[134:137], v[188:191], 0
	v_mfma_f32_16x16x32_bf16 v[118:121], v[142:145], v[188:191], 0
	v_mfma_f32_16x16x32_bf16 v[98:101], v[134:137], v[196:199], 0
	v_mfma_f32_16x16x32_bf16 v[94:97], v[142:145], v[196:199], 0
	v_mfma_f32_16x16x32_bf16 v[86:89], v[134:137], v[210:213], 0
	v_mfma_f32_16x16x32_bf16 v[78:81], v[142:145], v[210:213], 0
	v_mfma_f32_16x16x32_bf16 v[130:133], v[138:141], v[184:187], v[130:133]
	v_mfma_f32_16x16x32_bf16 v[126:129], v[146:149], v[184:187], v[126:129]
	v_mfma_f32_16x16x32_bf16 v[122:125], v[138:141], v[192:195], v[122:125]
	v_mfma_f32_16x16x32_bf16 v[118:121], v[146:149], v[192:195], v[118:121]
	v_mfma_f32_16x16x32_bf16 v[98:101], v[138:141], v[206:209], v[98:101]
	v_mfma_f32_16x16x32_bf16 v[94:97], v[146:149], v[206:209], v[94:97]
	v_mfma_f32_16x16x32_bf16 v[86:89], v[138:141], v[214:217], v[86:89]
	v_mfma_f32_16x16x32_bf16 v[78:81], v[146:149], v[214:217], v[78:81]
	s_setprio 0
	s_setprio 1
	v_mfma_f32_16x16x32_bf16 v[114:117], v[150:153], v[180:183], 0
	v_mfma_f32_16x16x32_bf16 v[110:113], v[166:169], v[180:183], 0
	v_mfma_f32_16x16x32_bf16 v[106:109], v[150:153], v[188:191], 0
	v_mfma_f32_16x16x32_bf16 v[102:105], v[166:169], v[188:191], 0
	v_mfma_f32_16x16x32_bf16 v[90:93], v[150:153], v[196:199], 0
	v_mfma_f32_16x16x32_bf16 v[82:85], v[166:169], v[196:199], 0
	v_mfma_f32_16x16x32_bf16 v[74:77], v[150:153], v[210:213], 0
	v_mfma_f32_16x16x32_bf16 v[70:73], v[166:169], v[210:213], 0
	v_mfma_f32_16x16x32_bf16 v[114:117], v[162:165], v[184:187], v[114:117]
	v_mfma_f32_16x16x32_bf16 v[110:113], v[176:179], v[184:187], v[110:113]
	v_mfma_f32_16x16x32_bf16 v[106:109], v[162:165], v[192:195], v[106:109]
	v_mfma_f32_16x16x32_bf16 v[102:105], v[176:179], v[192:195], v[102:105]
	v_mfma_f32_16x16x32_bf16 v[90:93], v[162:165], v[206:209], v[90:93]
	v_mfma_f32_16x16x32_bf16 v[82:85], v[176:179], v[206:209], v[82:85]
	s_setprio 2
	s_barrier
	v_mfma_f32_16x16x32_bf16 v[74:77], v[162:165], v[214:217], v[74:77]
	v_mfma_f32_16x16x32_bf16 v[70:73], v[176:179], v[214:217], v[70:73]
	s_setprio 0
	s_mov_b32 m0, s21
	v_lshl_add_u64 v[170:171], s[12:13], 0, v[0:1]
	s_add_u32 s8, s12, 0x158000
	ds_read_b128 v[180:183], v174 offset:16384
	ds_read_b128 v[184:187], v174 offset:17408
	ds_read_b128 v[188:191], v174 offset:18432
	ds_read_b128 v[192:195], v174 offset:19456
	ds_read_b128 v[196:199], v174 offset:20480
	ds_read_b128 v[206:209], v174 offset:21504
	ds_read_b128 v[210:213], v174 offset:22528
	ds_read_b128 v[214:217], v174 offset:23552
	global_load_lds_dwordx4 v[170:171], off
	v_lshl_add_u64 v[200:201], s[12:13], 0, v[156:157]
	s_mov_b32 m0, s22
	s_addc_u32 s9, s13, 0
	global_load_lds_dwordx4 v[200:201], off
	v_lshl_add_u64 v[218:219], s[8:9], 0, v[0:1]
	s_mov_b32 m0, s24
	v_lshl_add_u64 v[220:221], s[14:15], 0, v[154:155]
	global_load_lds_dwordx4 v[218:219], off
	v_lshl_add_u64 v[218:219], s[8:9], 0, v[156:157]
	s_mov_b32 m0, s25
	s_nop 0
	global_load_lds_dwordx4 v[218:219], off
	v_lshl_add_u64 v[218:219], s[14:15], 0, v[2:3]
	s_mov_b32 m0, s26
	s_nop 0
	global_load_lds_dwordx4 v[218:219], off
	s_mov_b32 m0, s30
	s_nop 0
	global_load_lds_dwordx4 v[220:221], off
	s_waitcnt vmcnt(8)
	s_waitcnt lgkmcnt(0)
	s_barrier
	s_setprio 1
	s_waitcnt lgkmcnt(0)
	v_mfma_f32_16x16x32_bf16 v[66:69], v[134:137], v[180:183], 0
	v_mfma_f32_16x16x32_bf16 v[62:65], v[142:145], v[180:183], 0
	v_mfma_f32_16x16x32_bf16 v[54:57], v[134:137], v[188:191], 0
	v_mfma_f32_16x16x32_bf16 v[46:49], v[142:145], v[188:191], 0
	v_mfma_f32_16x16x32_bf16 v[38:41], v[134:137], v[196:199], 0
	v_mfma_f32_16x16x32_bf16 v[30:33], v[142:145], v[196:199], 0
	v_mfma_f32_16x16x32_bf16 v[22:25], v[134:137], v[210:213], 0
	v_mfma_f32_16x16x32_bf16 v[14:17], v[142:145], v[210:213], 0
	v_mfma_f32_16x16x32_bf16 v[66:69], v[138:141], v[184:187], v[66:69]
	v_mfma_f32_16x16x32_bf16 v[62:65], v[146:149], v[184:187], v[62:65]
	v_mfma_f32_16x16x32_bf16 v[54:57], v[138:141], v[192:195], v[54:57]
	v_mfma_f32_16x16x32_bf16 v[46:49], v[146:149], v[192:195], v[46:49]
	v_mfma_f32_16x16x32_bf16 v[38:41], v[138:141], v[206:209], v[38:41]
	v_mfma_f32_16x16x32_bf16 v[30:33], v[146:149], v[206:209], v[30:33]
	v_mfma_f32_16x16x32_bf16 v[22:25], v[138:141], v[214:217], v[22:25]
	v_mfma_f32_16x16x32_bf16 v[14:17], v[146:149], v[214:217], v[14:17]
	s_setprio 0
	s_setprio 1
	v_mfma_f32_16x16x32_bf16 v[58:61], v[150:153], v[180:183], 0
	v_mfma_f32_16x16x32_bf16 v[50:53], v[166:169], v[180:183], 0
	v_mfma_f32_16x16x32_bf16 v[42:45], v[150:153], v[188:191], 0
	v_mfma_f32_16x16x32_bf16 v[34:37], v[166:169], v[188:191], 0
	v_mfma_f32_16x16x32_bf16 v[26:29], v[150:153], v[196:199], 0
	v_mfma_f32_16x16x32_bf16 v[18:21], v[166:169], v[196:199], 0
	v_mfma_f32_16x16x32_bf16 v[10:13], v[150:153], v[210:213], 0
	v_mfma_f32_16x16x32_bf16 v[6:9], v[166:169], v[210:213], 0
	v_mfma_f32_16x16x32_bf16 v[58:61], v[162:165], v[184:187], v[58:61]
	v_mfma_f32_16x16x32_bf16 v[50:53], v[176:179], v[184:187], v[50:53]
	v_mfma_f32_16x16x32_bf16 v[42:45], v[162:165], v[192:195], v[42:45]
	v_mfma_f32_16x16x32_bf16 v[34:37], v[176:179], v[192:195], v[34:37]
	v_mfma_f32_16x16x32_bf16 v[26:29], v[162:165], v[206:209], v[26:29]
	v_mfma_f32_16x16x32_bf16 v[18:21], v[176:179], v[206:209], v[18:21]
	s_setprio 2
	s_barrier
	v_mfma_f32_16x16x32_bf16 v[10:13], v[162:165], v[214:217], v[10:13]
	v_mfma_f32_16x16x32_bf16 v[6:9], v[176:179], v[214:217], v[6:9]
	s_setprio 0
	v_add_u32_e32 v146, s35, v172
	v_add_u32_e32 v175, s42, v172
	ds_read_b128 v[134:137], v146
	ds_read_b128 v[138:141], v146 offset:1024
	ds_read_b128 v[142:145], v146 offset:2048
	ds_read_b128 v[146:149], v146 offset:3072
	ds_read_b128 v[150:153], v175
	ds_read_b128 v[162:165], v175 offset:1024
	ds_read_b128 v[166:169], v175 offset:2048
	ds_read_b128 v[176:179], v175 offset:3072
	s_add_u32 s8, s14, 0x280000
	s_addc_u32 s9, s15, 0
	s_mov_b32 m0, s31
	v_lshl_add_u64 v[222:223], s[8:9], 0, v[2:3]
	ds_read_b128 v[180:183], v174 offset:32768
	ds_read_b128 v[184:187], v174 offset:33792
	ds_read_b128 v[188:191], v174 offset:34816
	ds_read_b128 v[192:195], v174 offset:35840
	ds_read_b128 v[196:199], v174 offset:36864
	ds_read_b128 v[206:209], v174 offset:37888
	ds_read_b128 v[210:213], v174 offset:38912
	ds_read_b128 v[214:217], v174 offset:39936
	global_load_lds_dwordx4 v[222:223], off
	v_lshl_add_u64 v[222:223], s[8:9], 0, v[154:155]
	s_mov_b32 m0, s34
	s_nop 0
	global_load_lds_dwordx4 v[222:223], off
	s_waitcnt vmcnt(8)
	s_waitcnt lgkmcnt(0)
	s_barrier
	s_setprio 1
	s_waitcnt lgkmcnt(0)
	v_mfma_f32_16x16x32_bf16 v[130:133], v[134:137], v[180:183], v[130:133]
	v_mfma_f32_16x16x32_bf16 v[126:129], v[142:145], v[180:183], v[126:129]
	v_mfma_f32_16x16x32_bf16 v[122:125], v[134:137], v[188:191], v[122:125]
	v_mfma_f32_16x16x32_bf16 v[118:121], v[142:145], v[188:191], v[118:121]
	v_mfma_f32_16x16x32_bf16 v[98:101], v[134:137], v[196:199], v[98:101]
	v_mfma_f32_16x16x32_bf16 v[94:97], v[142:145], v[196:199], v[94:97]
	v_mfma_f32_16x16x32_bf16 v[86:89], v[134:137], v[210:213], v[86:89]
	v_mfma_f32_16x16x32_bf16 v[78:81], v[142:145], v[210:213], v[78:81]
	v_mfma_f32_16x16x32_bf16 v[130:133], v[138:141], v[184:187], v[130:133]
	v_mfma_f32_16x16x32_bf16 v[126:129], v[146:149], v[184:187], v[126:129]
	v_mfma_f32_16x16x32_bf16 v[122:125], v[138:141], v[192:195], v[122:125]
	v_mfma_f32_16x16x32_bf16 v[118:121], v[146:149], v[192:195], v[118:121]
	v_mfma_f32_16x16x32_bf16 v[98:101], v[138:141], v[206:209], v[98:101]
	v_mfma_f32_16x16x32_bf16 v[94:97], v[146:149], v[206:209], v[94:97]
	v_mfma_f32_16x16x32_bf16 v[86:89], v[138:141], v[214:217], v[86:89]
	v_mfma_f32_16x16x32_bf16 v[78:81], v[146:149], v[214:217], v[78:81]
	s_setprio 0
	s_setprio 1
	v_mfma_f32_16x16x32_bf16 v[114:117], v[150:153], v[180:183], v[114:117]
	v_mfma_f32_16x16x32_bf16 v[110:113], v[166:169], v[180:183], v[110:113]
	v_mfma_f32_16x16x32_bf16 v[106:109], v[150:153], v[188:191], v[106:109]
	v_mfma_f32_16x16x32_bf16 v[102:105], v[166:169], v[188:191], v[102:105]
	v_mfma_f32_16x16x32_bf16 v[90:93], v[150:153], v[196:199], v[90:93]
	v_mfma_f32_16x16x32_bf16 v[82:85], v[166:169], v[196:199], v[82:85]
	v_mfma_f32_16x16x32_bf16 v[74:77], v[150:153], v[210:213], v[74:77]
	v_mfma_f32_16x16x32_bf16 v[70:73], v[166:169], v[210:213], v[70:73]
	v_mfma_f32_16x16x32_bf16 v[114:117], v[162:165], v[184:187], v[114:117]
	v_mfma_f32_16x16x32_bf16 v[110:113], v[176:179], v[184:187], v[110:113]
	v_mfma_f32_16x16x32_bf16 v[106:109], v[162:165], v[192:195], v[106:109]
	v_mfma_f32_16x16x32_bf16 v[102:105], v[176:179], v[192:195], v[102:105]
	v_mfma_f32_16x16x32_bf16 v[90:93], v[162:165], v[206:209], v[90:93]
	v_mfma_f32_16x16x32_bf16 v[82:85], v[176:179], v[206:209], v[82:85]
	s_setprio 2
	s_barrier
	v_mfma_f32_16x16x32_bf16 v[74:77], v[162:165], v[214:217], v[74:77]
	v_mfma_f32_16x16x32_bf16 v[70:73], v[176:179], v[214:217], v[70:73]
	s_setprio 0
	s_mov_b32 m0, s38
	v_lshl_add_u64 v[170:171], v[170:171], 0, s[28:29]
	s_add_u32 s8, s12, 0x158080
	ds_read_b128 v[180:183], v174 offset:49152
	ds_read_b128 v[184:187], v174 offset:50176
	ds_read_b128 v[188:191], v174 offset:51200
	ds_read_b128 v[192:195], v174 offset:52224
	ds_read_b128 v[196:199], v174 offset:53248
	ds_read_b128 v[206:209], v174 offset:54272
	ds_read_b128 v[210:213], v174 offset:55296
	ds_read_b128 v[214:217], v174 offset:56320
	global_load_lds_dwordx4 v[170:171], off
	v_lshl_add_u64 v[170:171], v[200:201], 0, s[28:29]
	s_mov_b32 m0, s39
	s_addc_u32 s9, s13, 0
	global_load_lds_dwordx4 v[170:171], off
	v_lshl_add_u64 v[170:171], s[8:9], 0, v[0:1]
	s_mov_b32 m0, s43
	s_nop 0
	global_load_lds_dwordx4 v[170:171], off
	v_lshl_add_u64 v[170:171], s[8:9], 0, v[156:157]
	s_mov_b32 m0, s44
	s_nop 0
	global_load_lds_dwordx4 v[170:171], off
	v_lshl_add_u64 v[170:171], v[218:219], 0, s[28:29]
	s_mov_b32 m0, s40
	s_nop 0
	global_load_lds_dwordx4 v[170:171], off
	v_lshl_add_u64 v[170:171], v[220:221], 0, s[28:29]
	s_mov_b32 m0, s41
	s_nop 0
	global_load_lds_dwordx4 v[170:171], off
	s_waitcnt vmcnt(8)
	s_waitcnt lgkmcnt(0)
	s_barrier
	s_setprio 1
	s_waitcnt lgkmcnt(0)
	v_mfma_f32_16x16x32_bf16 v[66:69], v[134:137], v[180:183], v[66:69]
	v_mfma_f32_16x16x32_bf16 v[62:65], v[142:145], v[180:183], v[62:65]
	v_mfma_f32_16x16x32_bf16 v[54:57], v[134:137], v[188:191], v[54:57]
	v_mfma_f32_16x16x32_bf16 v[46:49], v[142:145], v[188:191], v[46:49]
	v_mfma_f32_16x16x32_bf16 v[38:41], v[134:137], v[196:199], v[38:41]
	v_mfma_f32_16x16x32_bf16 v[30:33], v[142:145], v[196:199], v[30:33]
	v_mfma_f32_16x16x32_bf16 v[22:25], v[134:137], v[210:213], v[22:25]
	v_mfma_f32_16x16x32_bf16 v[14:17], v[142:145], v[210:213], v[14:17]
	v_mfma_f32_16x16x32_bf16 v[66:69], v[138:141], v[184:187], v[66:69]
	v_mfma_f32_16x16x32_bf16 v[62:65], v[146:149], v[184:187], v[62:65]
	v_mfma_f32_16x16x32_bf16 v[54:57], v[138:141], v[192:195], v[54:57]
	v_mfma_f32_16x16x32_bf16 v[46:49], v[146:149], v[192:195], v[46:49]
	v_mfma_f32_16x16x32_bf16 v[38:41], v[138:141], v[206:209], v[38:41]
	v_mfma_f32_16x16x32_bf16 v[30:33], v[146:149], v[206:209], v[30:33]
	v_mfma_f32_16x16x32_bf16 v[22:25], v[138:141], v[214:217], v[22:25]
	v_mfma_f32_16x16x32_bf16 v[14:17], v[146:149], v[214:217], v[14:17]
	s_setprio 0
	s_setprio 1
	v_mfma_f32_16x16x32_bf16 v[58:61], v[150:153], v[180:183], v[58:61]
	v_mfma_f32_16x16x32_bf16 v[50:53], v[166:169], v[180:183], v[50:53]
	v_mfma_f32_16x16x32_bf16 v[42:45], v[150:153], v[188:191], v[42:45]
	v_mfma_f32_16x16x32_bf16 v[34:37], v[166:169], v[188:191], v[34:37]
	v_mfma_f32_16x16x32_bf16 v[26:29], v[150:153], v[196:199], v[26:29]
	v_mfma_f32_16x16x32_bf16 v[18:21], v[166:169], v[196:199], v[18:21]
	v_mfma_f32_16x16x32_bf16 v[10:13], v[150:153], v[210:213], v[10:13]
	v_mfma_f32_16x16x32_bf16 v[6:9], v[166:169], v[210:213], v[6:9]
	v_mfma_f32_16x16x32_bf16 v[58:61], v[162:165], v[184:187], v[58:61]
	v_mfma_f32_16x16x32_bf16 v[50:53], v[176:179], v[184:187], v[50:53]
	v_mfma_f32_16x16x32_bf16 v[42:45], v[162:165], v[192:195], v[42:45]
	v_mfma_f32_16x16x32_bf16 v[34:37], v[176:179], v[192:195], v[34:37]
	v_mfma_f32_16x16x32_bf16 v[26:29], v[162:165], v[206:209], v[26:29]
	v_mfma_f32_16x16x32_bf16 v[18:21], v[176:179], v[206:209], v[18:21]
	s_setprio 2
	s_barrier
	v_mfma_f32_16x16x32_bf16 v[10:13], v[162:165], v[214:217], v[10:13]
	v_mfma_f32_16x16x32_bf16 v[6:9], v[176:179], v[214:217], v[6:9]
	s_setprio 0
	s_add_i32 s52, s52, 2
	s_add_u32 s50, s50, 0x100
	s_addc_u32 s51, s51, 0
	s_cmpk_gt_u32 s52, 0x53
	s_mov_b64 s[8:9], s[10:11]
	s_cbranch_scc0 .LBB0_2160
	s_branch .Lpeel_x__2160
